# GEMM K-loops (all 25): LDS-DMA via scalar-base addressing where the lane offset is 32-bit
# speedup vs baseline: 1.0037x; 1.0006x over previous
; #define PG8_STAGE(bufoff, gbase, voff) do { _Pragma("unroll") for (int _i = 0; _i < 2; ++_i) \
;         __builtin_amdgcn_global_load_lds((const unsigned*)((const char*)(gbase) + (voff)[_i]), (PG8_LAS unsigned*)(lds + (bufoff) + ldsw + _i * 8192), 16, 0, 0); } while (0)
; #define PG8_LDA(dst, b, h) do { if constexpr (DT != 1) { _Pragma("unroll") for (int m = 0; m < 4; ++m) _Pragma("unroll") for (int k = 0; k < 2; ++k) dst[m][k] = *(const PG8_LAS bf16x8*)(lds + PG8_SA(b, h) + aoff + m * 2048 + k * 1024); } \
;         else { _Pragma("unroll") for (int m = 0; m < 4; ++m) dst##8[m] = ld32(lds + PG8_SA(b, h) + aoff + m * 2048); } } while (0)
; #define PG8_LDB(dst, b, h) do { if constexpr (DT != 1) { _Pragma("unroll") for (int n = 0; n < 2; ++n) _Pragma("unroll") for (int k = 0; k < 2; ++k) dst[n][k] = *(const PG8_LAS bf16x8*)(lds + PG8_SB(b, h) + boff + n * 2048 + k * 1024); } \
;         else { _Pragma("unroll") for (int n = 0; n < 2; ++n) dst##8[n] = ld32(lds + PG8_SB(b, h) + boff + n * 2048); } } while (0)
; #define PG8_WAIT_V(n) asm volatile("s_waitcnt vmcnt(" #n ")" ::: "memory")
; #define PG8_WAIT_L(n) asm volatile("s_waitcnt lgkmcnt(" #n ")" ::: "memory")
; #define PG8_BAR __builtin_amdgcn_s_barrier()
; #define PG8_SCHED __builtin_amdgcn_sched_barrier(0)
;     ...
;             PG8_LDB(B0, 0, 0); PG8_LDB(B1, 0, 1); PG8_SCHED; PG8_LDA(At, 0, 0); PG8_STAGE(PG8_SA(1, 1), a1 + hstepA, voffA);
;             PG8_WAIT_V(8); PG8_WAIT_L(0); PG8_BAR; PG8_MMA(0, 0, At, B0); PG8_MMA(0, 1, At, B1); PG8_BAR; PG8_SCHED;
;             PG8_LDA(At, 0, 1); PG8_STAGE(PG8_SB(0, 0), b2, voffB); PG8_STAGE(PG8_SB(0, 1), b2 + hstepB, voffB); PG8_STAGE(PG8_SA(0, 0), a2, voffA);
;             PG8_WAIT_V(8); PG8_WAIT_L(0); PG8_BAR; PG8_MMA(1, 0, At, B0); PG8_MMA(1, 1, At, B1); PG8_BAR; PG8_SCHED;
.LBB0_303:
	ds_read_b128 v[146:149], v159
	ds_read_b128 v[150:153], v159 offset:1024
	ds_read_b128 v[154:157], v159 offset:2048
	ds_read_b128 v[164:167], v159 offset:3072
	ds_read_b128 v[168:171], v160
	ds_read_b128 v[172:175], v160 offset:1024
	ds_read_b128 v[176:179], v160 offset:2048
	ds_read_b128 v[180:183], v160 offset:3072
	s_add_i32 s69, s34, 2
	s_add_u32 s30, s28, 0x100
	s_addc_u32 s31, s29, 0
	s_cmp_eq_u32 s60, s34
	s_cselect_b32 s34, s26, s67
	s_cselect_b32 s37, s3, s31
	s_cselect_b32 s36, s2, s30
	s_cselect_b32 s35, s27, s68
	v_lshl_add_u64 v[216:217], s[28:29], 0, v[140:141]
	s_add_i32 m0, s48, 0xc000
	ds_read_b128 v[184:187], v161
	ds_read_b128 v[188:191], v161 offset:1024
	ds_read_b128 v[192:195], v161 offset:2048
	ds_read_b128 v[196:199], v161 offset:3072
	ds_read_b128 v[200:203], v161 offset:4096
	ds_read_b128 v[204:207], v161 offset:5120
	ds_read_b128 v[208:211], v161 offset:6144
	ds_read_b128 v[212:215], v161 offset:7168
	global_load_lds_dwordx4 v[216:217], off
	v_lshl_add_u64 v[216:217], s[28:29], 0, v[138:139]
	s_add_i32 m0, s48, 0xe000
	s_nop 0
	global_load_lds_dwordx4 v[216:217], off
	s_waitcnt vmcnt(8)
	s_waitcnt lgkmcnt(0)
	s_barrier
	s_setprio 1
	s_waitcnt lgkmcnt(0)
	v_mfma_f32_16x16x32_bf16 v[126:129], v[146:149], v[184:187], v[126:129]
	v_mfma_f32_16x16x32_bf16 v[122:125], v[154:157], v[184:187], v[122:125]
	v_mfma_f32_16x16x32_bf16 v[118:121], v[146:149], v[192:195], v[118:121]
	v_mfma_f32_16x16x32_bf16 v[114:117], v[154:157], v[192:195], v[114:117]
	v_mfma_f32_16x16x32_bf16 v[106:109], v[146:149], v[200:203], v[106:109]
	v_mfma_f32_16x16x32_bf16 v[98:101], v[154:157], v[200:203], v[98:101]
	v_mfma_f32_16x16x32_bf16 v[90:93], v[146:149], v[208:211], v[90:93]
	v_mfma_f32_16x16x32_bf16 v[82:85], v[154:157], v[208:211], v[82:85]
	v_mfma_f32_16x16x32_bf16 v[126:129], v[150:153], v[188:191], v[126:129]
	v_mfma_f32_16x16x32_bf16 v[122:125], v[164:167], v[188:191], v[122:125]
	v_mfma_f32_16x16x32_bf16 v[118:121], v[150:153], v[196:199], v[118:121]
	v_mfma_f32_16x16x32_bf16 v[114:117], v[164:167], v[196:199], v[114:117]
	v_mfma_f32_16x16x32_bf16 v[106:109], v[150:153], v[204:207], v[106:109]
	v_mfma_f32_16x16x32_bf16 v[98:101], v[164:167], v[204:207], v[98:101]
	v_mfma_f32_16x16x32_bf16 v[90:93], v[150:153], v[212:215], v[90:93]
	v_mfma_f32_16x16x32_bf16 v[82:85], v[164:167], v[212:215], v[82:85]
	s_setprio 0
	s_setprio 1
	v_mfma_f32_16x16x32_bf16 v[110:113], v[168:171], v[184:187], v[110:113]
	v_mfma_f32_16x16x32_bf16 v[102:105], v[176:179], v[184:187], v[102:105]
	v_mfma_f32_16x16x32_bf16 v[94:97], v[168:171], v[192:195], v[94:97]
	v_mfma_f32_16x16x32_bf16 v[86:89], v[176:179], v[192:195], v[86:89]
	v_mfma_f32_16x16x32_bf16 v[78:81], v[168:171], v[200:203], v[78:81]
	v_mfma_f32_16x16x32_bf16 v[74:77], v[176:179], v[200:203], v[74:77]
	v_mfma_f32_16x16x32_bf16 v[70:73], v[168:171], v[208:211], v[70:73]
	v_mfma_f32_16x16x32_bf16 v[66:69], v[176:179], v[208:211], v[66:69]
	v_mfma_f32_16x16x32_bf16 v[110:113], v[172:175], v[188:191], v[110:113]
	v_mfma_f32_16x16x32_bf16 v[102:105], v[180:183], v[188:191], v[102:105]
	v_mfma_f32_16x16x32_bf16 v[94:97], v[172:175], v[196:199], v[94:97]
	v_mfma_f32_16x16x32_bf16 v[86:89], v[180:183], v[196:199], v[86:89]
	v_mfma_f32_16x16x32_bf16 v[78:81], v[172:175], v[204:207], v[78:81]
	v_mfma_f32_16x16x32_bf16 v[74:77], v[180:183], v[204:207], v[74:77]
	v_mfma_f32_16x16x32_bf16 v[70:73], v[172:175], v[212:215], v[70:73]
	v_mfma_f32_16x16x32_bf16 v[66:69], v[180:183], v[212:215], v[66:69]
	s_setprio 0
	s_barrier
	s_mov_b32 m0, s44
	s_add_u32 s98, s34, 0x80
	s_addc_u32 s99, s35, 0
	s_add_u32 s28, s34, 0x160000
	ds_read_b128 v[184:187], v161 offset:16384
	ds_read_b128 v[188:191], v161 offset:17408
	ds_read_b128 v[192:195], v161 offset:18432
	ds_read_b128 v[196:199], v161 offset:19456
	ds_read_b128 v[200:203], v161 offset:20480
	ds_read_b128 v[204:207], v161 offset:21504
	ds_read_b128 v[208:211], v161 offset:22528
	ds_read_b128 v[212:215], v161 offset:23552
	global_load_lds_dwordx4 v132, s[34:35]
	s_mov_b32 m0, s45
	s_addc_u32 s29, s35, 0
	global_load_lds_dwordx4 v136, s[34:35]
	s_mov_b32 m0, s46
	s_nop 0
	global_load_lds_dwordx4 v132, s[28:29]
	s_mov_b32 m0, s47
	s_nop 0
	global_load_lds_dwordx4 v136, s[28:29]
	s_add_u32 s100, s36, 0x80
	s_addc_u32 s101, s37, 0
	s_mov_b32 m0, s48
	s_nop 0
	global_load_lds_dwordx4 v130, s[36:37]
	s_mov_b32 m0, s49
	s_nop 0
	global_load_lds_dwordx4 v134, s[36:37]
	s_waitcnt vmcnt(8)
	s_waitcnt lgkmcnt(0)
	s_barrier
	s_setprio 1
	s_waitcnt lgkmcnt(0)
	v_mfma_f32_16x16x32_bf16 v[62:65], v[146:149], v[184:187], v[62:65]
	v_mfma_f32_16x16x32_bf16 v[58:61], v[154:157], v[184:187], v[58:61]
	v_mfma_f32_16x16x32_bf16 v[54:57], v[146:149], v[192:195], v[54:57]
	v_mfma_f32_16x16x32_bf16 v[50:53], v[154:157], v[192:195], v[50:53]
	v_mfma_f32_16x16x32_bf16 v[42:45], v[146:149], v[200:203], v[42:45]
	v_mfma_f32_16x16x32_bf16 v[34:37], v[154:157], v[200:203], v[34:37]
	v_mfma_f32_16x16x32_bf16 v[26:29], v[146:149], v[208:211], v[26:29]
	v_mfma_f32_16x16x32_bf16 v[18:21], v[154:157], v[208:211], v[18:21]
	v_mfma_f32_16x16x32_bf16 v[62:65], v[150:153], v[188:191], v[62:65]
	v_mfma_f32_16x16x32_bf16 v[58:61], v[164:167], v[188:191], v[58:61]
	v_mfma_f32_16x16x32_bf16 v[54:57], v[150:153], v[196:199], v[54:57]
	v_mfma_f32_16x16x32_bf16 v[50:53], v[164:167], v[196:199], v[50:53]
	v_mfma_f32_16x16x32_bf16 v[42:45], v[150:153], v[204:207], v[42:45]
	v_mfma_f32_16x16x32_bf16 v[34:37], v[164:167], v[204:207], v[34:37]
	v_mfma_f32_16x16x32_bf16 v[26:29], v[150:153], v[212:215], v[26:29]
	v_mfma_f32_16x16x32_bf16 v[18:21], v[164:167], v[212:215], v[18:21]
	s_setprio 0
	s_setprio 1
	v_mfma_f32_16x16x32_bf16 v[46:49], v[168:171], v[184:187], v[46:49]
	v_mfma_f32_16x16x32_bf16 v[38:41], v[176:179], v[184:187], v[38:41]
	v_mfma_f32_16x16x32_bf16 v[30:33], v[168:171], v[192:195], v[30:33]
	v_mfma_f32_16x16x32_bf16 v[22:25], v[176:179], v[192:195], v[22:25]
	v_mfma_f32_16x16x32_bf16 v[14:17], v[168:171], v[200:203], v[14:17]
	v_mfma_f32_16x16x32_bf16 v[10:13], v[176:179], v[200:203], v[10:13]
	v_mfma_f32_16x16x32_bf16 v[6:9], v[168:171], v[208:211], v[6:9]
	v_mfma_f32_16x16x32_bf16 v[2:5], v[176:179], v[208:211], v[2:5]
	v_mfma_f32_16x16x32_bf16 v[46:49], v[172:175], v[188:191], v[46:49]
	v_mfma_f32_16x16x32_bf16 v[38:41], v[180:183], v[188:191], v[38:41]
	v_mfma_f32_16x16x32_bf16 v[30:33], v[172:175], v[196:199], v[30:33]
	v_mfma_f32_16x16x32_bf16 v[22:25], v[180:183], v[196:199], v[22:25]
	v_mfma_f32_16x16x32_bf16 v[14:17], v[172:175], v[204:207], v[14:17]
	v_mfma_f32_16x16x32_bf16 v[10:13], v[180:183], v[204:207], v[10:13]
	v_mfma_f32_16x16x32_bf16 v[6:9], v[172:175], v[212:215], v[6:9]
	v_mfma_f32_16x16x32_bf16 v[2:5], v[180:183], v[212:215], v[2:5]
	s_setprio 0
	s_barrier
; #define PG8_STAGE(bufoff, gbase, voff) do { _Pragma("unroll") for (int _i = 0; _i < 2; ++_i) \
;         __builtin_amdgcn_global_load_lds((const unsigned*)((const char*)(gbase) + (voff)[_i]), (PG8_LAS unsigned*)(lds + (bufoff) + ldsw + _i * 8192), 16, 0, 0); } while (0)
; #define PG8_LDA(dst, b, h) do { if constexpr (DT != 1) { _Pragma("unroll") for (int m = 0; m < 4; ++m) _Pragma("unroll") for (int k = 0; k < 2; ++k) dst[m][k] = *(const PG8_LAS bf16x8*)(lds + PG8_SA(b, h) + aoff + m * 2048 + k * 1024); } \
;         else { _Pragma("unroll") for (int m = 0; m < 4; ++m) dst##8[m] = ld32(lds + PG8_SA(b, h) + aoff + m * 2048); } } while (0)
; #define PG8_LDB(dst, b, h) do { if constexpr (DT != 1) { _Pragma("unroll") for (int n = 0; n < 2; ++n) _Pragma("unroll") for (int k = 0; k < 2; ++k) dst[n][k] = *(const PG8_LAS bf16x8*)(lds + PG8_SB(b, h) + boff + n * 2048 + k * 1024); } \
;         else { _Pragma("unroll") for (int n = 0; n < 2; ++n) dst##8[n] = ld32(lds + PG8_SB(b, h) + boff + n * 2048); } } while (0)
; #define PG8_WAIT_V(n) asm volatile("s_waitcnt vmcnt(" #n ")" ::: "memory")
; #define PG8_WAIT_L(n) asm volatile("s_waitcnt lgkmcnt(" #n ")" ::: "memory")
; #define PG8_BAR __builtin_amdgcn_s_barrier()
; #define PG8_SCHED __builtin_amdgcn_sched_barrier(0)
;     ...
;             PG8_LDB(B0, 1, 0); PG8_LDB(B1, 1, 1); PG8_SCHED; PG8_LDA(At, 1, 0); PG8_STAGE(PG8_SA(0, 1), a2 + hstepA, voffA);
;             PG8_WAIT_V(8); PG8_WAIT_L(0); PG8_BAR; PG8_MMA(0, 0, At, B0); PG8_MMA(0, 1, At, B1); PG8_BAR; PG8_SCHED;
;             PG8_LDA(At, 1, 1); PG8_STAGE(PG8_SB(1, 0), b3, voffB); PG8_STAGE(PG8_SB(1, 1), b3 + hstepB, voffB); PG8_STAGE(PG8_SA(1, 0), a3, voffA);
;             PG8_WAIT_V(8); PG8_WAIT_L(0); PG8_BAR; PG8_MMA(1, 0, At, B0); PG8_MMA(1, 1, At, B1); PG8_BAR; PG8_SCHED;
	ds_read_b128 v[146:149], v162
	ds_read_b128 v[150:153], v162 offset:1024
	ds_read_b128 v[154:157], v162 offset:2048
	ds_read_b128 v[164:167], v162 offset:3072
	ds_read_b128 v[168:171], v163
	ds_read_b128 v[172:175], v163 offset:1024
	ds_read_b128 v[176:179], v163 offset:2048
	ds_read_b128 v[180:183], v163 offset:3072
	s_add_u32 s28, s36, 0x160000
	s_addc_u32 s29, s37, 0
	s_mov_b32 m0, s50
	ds_read_b128 v[184:187], v161 offset:32768
	ds_read_b128 v[188:191], v161 offset:33792
	ds_read_b128 v[192:195], v161 offset:34816
	ds_read_b128 v[196:199], v161 offset:35840
	ds_read_b128 v[200:203], v161 offset:36864
	ds_read_b128 v[204:207], v161 offset:37888
	ds_read_b128 v[208:211], v161 offset:38912
	ds_read_b128 v[212:215], v161 offset:39936
	global_load_lds_dwordx4 v130, s[28:29]
	s_mov_b32 m0, s51
	s_nop 0
	global_load_lds_dwordx4 v134, s[28:29]
	s_waitcnt vmcnt(8)
	s_waitcnt lgkmcnt(0)
	s_barrier
	s_setprio 1
	s_waitcnt lgkmcnt(0)
	v_mfma_f32_16x16x32_bf16 v[126:129], v[146:149], v[184:187], v[126:129]
	v_mfma_f32_16x16x32_bf16 v[122:125], v[154:157], v[184:187], v[122:125]
	v_mfma_f32_16x16x32_bf16 v[118:121], v[146:149], v[192:195], v[118:121]
	v_mfma_f32_16x16x32_bf16 v[114:117], v[154:157], v[192:195], v[114:117]
	v_mfma_f32_16x16x32_bf16 v[106:109], v[146:149], v[200:203], v[106:109]
	v_mfma_f32_16x16x32_bf16 v[98:101], v[154:157], v[200:203], v[98:101]
	v_mfma_f32_16x16x32_bf16 v[90:93], v[146:149], v[208:211], v[90:93]
	v_mfma_f32_16x16x32_bf16 v[82:85], v[154:157], v[208:211], v[82:85]
	v_mfma_f32_16x16x32_bf16 v[126:129], v[150:153], v[188:191], v[126:129]
	v_mfma_f32_16x16x32_bf16 v[122:125], v[164:167], v[188:191], v[122:125]
	v_mfma_f32_16x16x32_bf16 v[118:121], v[150:153], v[196:199], v[118:121]
	v_mfma_f32_16x16x32_bf16 v[114:117], v[164:167], v[196:199], v[114:117]
	v_mfma_f32_16x16x32_bf16 v[106:109], v[150:153], v[204:207], v[106:109]
	v_mfma_f32_16x16x32_bf16 v[98:101], v[164:167], v[204:207], v[98:101]
	v_mfma_f32_16x16x32_bf16 v[90:93], v[150:153], v[212:215], v[90:93]
	v_mfma_f32_16x16x32_bf16 v[82:85], v[164:167], v[212:215], v[82:85]
	s_setprio 0
	s_setprio 1
	v_mfma_f32_16x16x32_bf16 v[110:113], v[168:171], v[184:187], v[110:113]
	v_mfma_f32_16x16x32_bf16 v[102:105], v[176:179], v[184:187], v[102:105]
	v_mfma_f32_16x16x32_bf16 v[94:97], v[168:171], v[192:195], v[94:97]
	v_mfma_f32_16x16x32_bf16 v[86:89], v[176:179], v[192:195], v[86:89]
	v_mfma_f32_16x16x32_bf16 v[78:81], v[168:171], v[200:203], v[78:81]
	v_mfma_f32_16x16x32_bf16 v[74:77], v[176:179], v[200:203], v[74:77]
	v_mfma_f32_16x16x32_bf16 v[70:73], v[168:171], v[208:211], v[70:73]
	v_mfma_f32_16x16x32_bf16 v[66:69], v[176:179], v[208:211], v[66:69]
	v_mfma_f32_16x16x32_bf16 v[110:113], v[172:175], v[188:191], v[110:113]
	v_mfma_f32_16x16x32_bf16 v[102:105], v[180:183], v[188:191], v[102:105]
	v_mfma_f32_16x16x32_bf16 v[94:97], v[172:175], v[196:199], v[94:97]
	v_mfma_f32_16x16x32_bf16 v[86:89], v[180:183], v[196:199], v[86:89]
	v_mfma_f32_16x16x32_bf16 v[78:81], v[172:175], v[204:207], v[78:81]
	v_mfma_f32_16x16x32_bf16 v[74:77], v[180:183], v[204:207], v[74:77]
	v_mfma_f32_16x16x32_bf16 v[70:73], v[172:175], v[212:215], v[70:73]
	v_mfma_f32_16x16x32_bf16 v[66:69], v[180:183], v[212:215], v[66:69]
	s_setprio 0
	s_barrier
	s_mov_b32 m0, s54
	s_add_u32 s28, s34, 0x160080
	ds_read_b128 v[184:187], v161 offset:49152
	ds_read_b128 v[188:191], v161 offset:50176
	ds_read_b128 v[192:195], v161 offset:51200
	ds_read_b128 v[196:199], v161 offset:52224
	ds_read_b128 v[200:203], v161 offset:53248
	ds_read_b128 v[204:207], v161 offset:54272
	ds_read_b128 v[208:211], v161 offset:55296
	ds_read_b128 v[212:215], v161 offset:56320
	global_load_lds_dwordx4 v132, s[98:99]
	s_mov_b32 m0, s55
	s_addc_u32 s29, s35, 0
	global_load_lds_dwordx4 v136, s[98:99]
	s_mov_b32 m0, s58
	s_nop 0
	global_load_lds_dwordx4 v132, s[28:29]
	s_mov_b32 m0, s59
	s_nop 0
	global_load_lds_dwordx4 v136, s[28:29]
	s_mov_b32 m0, s56
	s_nop 0
	global_load_lds_dwordx4 v130, s[100:101]
	s_mov_b32 m0, s57
	s_nop 0
	global_load_lds_dwordx4 v134, s[100:101]
	s_waitcnt vmcnt(8)
	s_waitcnt lgkmcnt(0)
	s_barrier
; #define PG8_WAIT_V(n) asm volatile("s_waitcnt vmcnt(" #n ")" ::: "memory")
; #define PG8_WAIT_L(n) asm volatile("s_waitcnt lgkmcnt(" #n ")" ::: "memory")
; #define PG8_BAR __builtin_amdgcn_s_barrier()
; #define PG8_SCHED __builtin_amdgcn_sched_barrier(0)
;     __device__ __forceinline__ void operator()(const f32x4 (&acc)[2][2][4][2], const Unit& u, int wr, int wc, int fr, int fq) const {
;     ...
;                 for (int m = 0; m < 4; ++m) { const size_t off = (size_t)(row0 + ai * HALF + m * 16) * ldc + col0;
; #pragma unroll
;                     for (int bj = 0; bj < 2; ++bj) { const h16x8_t w = wv[m][bj];
;                         const f32x4 b0 = (f32x4){(float)w[0], (float)w[1], (float)w[2], (float)w[3]}, b1 = (f32x4){(float)w[4], (float)w[5], (float)w[6], (float)w[7]};
;                         const f32x4 o0 = b0 + acc[ai][bj][m][0] * s, o1 = b1 + acc[ai][bj][m][1] * s;
;     ...
;             PG8_WAIT_V(8); PG8_WAIT_L(0); PG8_BAR; PG8_MMA(1, 0, At, B0); PG8_MMA(1, 1, At, B1); PG8_BAR; PG8_SCHED;
	s_setprio 1
	s_waitcnt lgkmcnt(0)
	v_mfma_f32_16x16x32_bf16 v[62:65], v[146:149], v[184:187], v[62:65]
	v_mfma_f32_16x16x32_bf16 v[58:61], v[154:157], v[184:187], v[58:61]
	v_mfma_f32_16x16x32_bf16 v[54:57], v[146:149], v[192:195], v[54:57]
	v_mfma_f32_16x16x32_bf16 v[50:53], v[154:157], v[192:195], v[50:53]
	v_mfma_f32_16x16x32_bf16 v[42:45], v[146:149], v[200:203], v[42:45]
	v_mfma_f32_16x16x32_bf16 v[34:37], v[154:157], v[200:203], v[34:37]
	v_mfma_f32_16x16x32_bf16 v[26:29], v[146:149], v[208:211], v[26:29]
	v_mfma_f32_16x16x32_bf16 v[18:21], v[154:157], v[208:211], v[18:21]
	v_mfma_f32_16x16x32_bf16 v[62:65], v[150:153], v[188:191], v[62:65]
	v_mfma_f32_16x16x32_bf16 v[58:61], v[164:167], v[188:191], v[58:61]
	v_mfma_f32_16x16x32_bf16 v[54:57], v[150:153], v[196:199], v[54:57]
	v_mfma_f32_16x16x32_bf16 v[50:53], v[164:167], v[196:199], v[50:53]
	v_mfma_f32_16x16x32_bf16 v[42:45], v[150:153], v[204:207], v[42:45]
	v_mfma_f32_16x16x32_bf16 v[34:37], v[164:167], v[204:207], v[34:37]
	v_mfma_f32_16x16x32_bf16 v[26:29], v[150:153], v[212:215], v[26:29]
	v_mfma_f32_16x16x32_bf16 v[18:21], v[164:167], v[212:215], v[18:21]
	s_setprio 0
	s_setprio 1
	v_mfma_f32_16x16x32_bf16 v[46:49], v[168:171], v[184:187], v[46:49]
	v_mfma_f32_16x16x32_bf16 v[38:41], v[176:179], v[184:187], v[38:41]
	v_mfma_f32_16x16x32_bf16 v[30:33], v[168:171], v[192:195], v[30:33]
	v_mfma_f32_16x16x32_bf16 v[22:25], v[176:179], v[192:195], v[22:25]
	v_mfma_f32_16x16x32_bf16 v[14:17], v[168:171], v[200:203], v[14:17]
	v_mfma_f32_16x16x32_bf16 v[10:13], v[176:179], v[200:203], v[10:13]
	v_mfma_f32_16x16x32_bf16 v[6:9], v[168:171], v[208:211], v[6:9]
	v_mfma_f32_16x16x32_bf16 v[2:5], v[176:179], v[208:211], v[2:5]
	v_mfma_f32_16x16x32_bf16 v[46:49], v[172:175], v[188:191], v[46:49]
	v_mfma_f32_16x16x32_bf16 v[38:41], v[180:183], v[188:191], v[38:41]
	v_mfma_f32_16x16x32_bf16 v[30:33], v[172:175], v[196:199], v[30:33]
	v_mfma_f32_16x16x32_bf16 v[22:25], v[180:183], v[196:199], v[22:25]
	v_mfma_f32_16x16x32_bf16 v[14:17], v[172:175], v[204:207], v[14:17]
	v_mfma_f32_16x16x32_bf16 v[10:13], v[180:183], v[204:207], v[10:13]
	v_mfma_f32_16x16x32_bf16 v[6:9], v[172:175], v[212:215], v[6:9]
	v_mfma_f32_16x16x32_bf16 v[2:5], v[180:183], v[212:215], v[2:5]
	s_setprio 0
	s_barrier
	s_add_u32 s67, s67, 0x100
	s_addc_u32 s68, s68, 0
	s_cmp_ge_i32 s69, s53
	s_mov_b64 s[28:29], s[30:31]
	s_mov_b32 s34, s69
	s_cbranch_scc0 .LBB0_303
	v_pk_mul_f32 v[128:129], v[128:129], 0.5 op_sel_hi:[1,0]
	v_pk_mul_f32 v[126:127], v[126:127], 0.5 op_sel_hi:[1,0]
	v_pk_mul_f32 v[146:147], v[124:125], 0.5 op_sel_hi:[1,0]
	v_pk_mul_f32 v[148:149], v[122:123], 0.5 op_sel_hi:[1,0]
	v_pk_mul_f32 v[150:151], v[112:113], 0.5 op_sel_hi:[1,0]
	v_pk_mul_f32 v[152:153], v[110:111], 0.5 op_sel_hi:[1,0]
	v_pk_mul_f32 v[154:155], v[104:105], 0.5 op_sel_hi:[1,0]
	v_pk_mul_f32 v[156:157], v[102:103], 0.5 op_sel_hi:[1,0]
	v_pk_mul_f32 v[110:111], v[120:121], 0.5 op_sel_hi:[1,0]
	v_pk_mul_f32 v[112:113], v[118:119], 0.5 op_sel_hi:[1,0]
	v_pk_mul_f32 v[116:117], v[116:117], 0.5 op_sel_hi:[1,0]
	v_pk_mul_f32 v[114:115], v[114:115], 0.5 op_sel_hi:[1,0]
	v_pk_mul_f32 v[118:119], v[96:97], 0.5 op_sel_hi:[1,0]
	v_pk_mul_f32 v[120:121], v[94:95], 0.5 op_sel_hi:[1,0]
	v_pk_mul_f32 v[122:123], v[88:89], 0.5 op_sel_hi:[1,0]
	v_pk_mul_f32 v[124:125], v[86:87], 0.5 op_sel_hi:[1,0]
	v_pk_mul_f32 v[94:95], v[108:109], 0.5 op_sel_hi:[1,0]
	v_pk_mul_f32 v[96:97], v[106:107], 0.5 op_sel_hi:[1,0]
	v_pk_mul_f32 v[100:101], v[100:101], 0.5 op_sel_hi:[1,0]
	v_pk_mul_f32 v[98:99], v[98:99], 0.5 op_sel_hi:[1,0]
	v_pk_mul_f32 v[102:103], v[80:81], 0.5 op_sel_hi:[1,0]
	v_pk_mul_f32 v[104:105], v[78:79], 0.5 op_sel_hi:[1,0]
	v_pk_mul_f32 v[106:107], v[76:77], 0.5 op_sel_hi:[1,0]
	v_pk_mul_f32 v[108:109], v[74:75], 0.5 op_sel_hi:[1,0]
	v_pk_mul_f32 v[74:75], v[92:93], 0.5 op_sel_hi:[1,0]
	v_pk_mul_f32 v[76:77], v[90:91], 0.5 op_sel_hi:[1,0]
	v_pk_mul_f32 v[78:79], v[84:85], 0.5 op_sel_hi:[1,0]
	v_pk_mul_f32 v[80:81], v[82:83], 0.5 op_sel_hi:[1,0]
	v_pk_mul_f32 v[86:87], v[72:73], 0.5 op_sel_hi:[1,0]
	v_pk_mul_f32 v[88:89], v[70:71], 0.5 op_sel_hi:[1,0]
	v_pk_mul_f32 v[90:91], v[68:69], 0.5 op_sel_hi:[1,0]
	v_pk_mul_f32 v[92:93], v[66:67], 0.5 op_sel_hi:[1,0]
	v_pk_mul_f32 v[64:65], v[64:65], 0.5 op_sel_hi:[1,0]
	v_pk_mul_f32 v[62:63], v[62:63], 0.5 op_sel_hi:[1,0]
	v_pk_mul_f32 v[66:67], v[60:61], 0.5 op_sel_hi:[1,0]
	v_pk_mul_f32 v[68:69], v[58:59], 0.5 op_sel_hi:[1,0]
	v_pk_mul_f32 v[70:71], v[48:49], 0.5 op_sel_hi:[1,0]
	v_pk_mul_f32 v[72:73], v[46:47], 0.5 op_sel_hi:[1,0]
	v_pk_mul_f32 v[82:83], v[40:41], 0.5 op_sel_hi:[1,0]
	v_pk_mul_f32 v[84:85], v[38:39], 0.5 op_sel_hi:[1,0]
	v_pk_mul_f32 v[46:47], v[56:57], 0.5 op_sel_hi:[1,0]
	v_pk_mul_f32 v[48:49], v[54:55], 0.5 op_sel_hi:[1,0]
	v_pk_mul_f32 v[52:53], v[52:53], 0.5 op_sel_hi:[1,0]
	v_pk_mul_f32 v[50:51], v[50:51], 0.5 op_sel_hi:[1,0]
	v_pk_mul_f32 v[54:55], v[32:33], 0.5 op_sel_hi:[1,0]
	v_pk_mul_f32 v[56:57], v[30:31], 0.5 op_sel_hi:[1,0]
	v_pk_mul_f32 v[58:59], v[24:25], 0.5 op_sel_hi:[1,0]
	v_pk_mul_f32 v[60:61], v[22:23], 0.5 op_sel_hi:[1,0]
	v_pk_mul_f32 v[22:23], v[44:45], 0.5 op_sel_hi:[1,0]
	v_pk_mul_f32 v[24:25], v[42:43], 0.5 op_sel_hi:[1,0]
	v_pk_mul_f32 v[30:31], v[36:37], 0.5 op_sel_hi:[1,0]
	v_pk_mul_f32 v[32:33], v[34:35], 0.5 op_sel_hi:[1,0]
	v_pk_mul_f32 v[34:35], v[16:17], 0.5 op_sel_hi:[1,0]
	v_pk_mul_f32 v[36:37], v[14:15], 0.5 op_sel_hi:[1,0]
	v_pk_mul_f32 v[38:39], v[12:13], 0.5 op_sel_hi:[1,0]
	v_pk_mul_f32 v[40:41], v[10:11], 0.5 op_sel_hi:[1,0]
	v_pk_mul_f32 v[10:11], v[28:29], 0.5 op_sel_hi:[1,0]
	v_pk_mul_f32 v[12:13], v[26:27], 0.5 op_sel_hi:[1,0]
	v_pk_mul_f32 v[14:15], v[20:21], 0.5 op_sel_hi:[1,0]
	v_pk_mul_f32 v[16:17], v[18:19], 0.5 op_sel_hi:[1,0]
	v_pk_mul_f32 v[8:9], v[8:9], 0.5 op_sel_hi:[1,0]
	v_pk_mul_f32 v[6:7], v[6:7], 0.5 op_sel_hi:[1,0]
	v_pk_mul_f32 v[4:5], v[4:5], 0.5 op_sel_hi:[1,0]
	v_pk_mul_f32 v[2:3], v[2:3], 0.5 op_sel_hi:[1,0]

; #define PG8_STAGE(bufoff, gbase, voff) do { _Pragma("unroll") for (int _i = 0; _i < 2; ++_i) \
;         __builtin_amdgcn_global_load_lds((const unsigned*)((const char*)(gbase) + (voff)[_i]), (PG8_LAS unsigned*)(lds + (bufoff) + ldsw + _i * 8192), 16, 0, 0); } while (0)
; #define PG8_LDA(dst, b, h) do { if constexpr (DT != 1) { _Pragma("unroll") for (int m = 0; m < 4; ++m) _Pragma("unroll") for (int k = 0; k < 2; ++k) dst[m][k] = *(const PG8_LAS bf16x8*)(lds + PG8_SA(b, h) + aoff + m * 2048 + k * 1024); } \
;         else { _Pragma("unroll") for (int m = 0; m < 4; ++m) dst##8[m] = ld32(lds + PG8_SA(b, h) + aoff + m * 2048); } } while (0)
; #define PG8_LDB(dst, b, h) do { if constexpr (DT != 1) { _Pragma("unroll") for (int n = 0; n < 2; ++n) _Pragma("unroll") for (int k = 0; k < 2; ++k) dst[n][k] = *(const PG8_LAS bf16x8*)(lds + PG8_SB(b, h) + boff + n * 2048 + k * 1024); } \
;         else { _Pragma("unroll") for (int n = 0; n < 2; ++n) dst##8[n] = ld32(lds + PG8_SB(b, h) + boff + n * 2048); } } while (0)
; #define PG8_WAIT_V(n) asm volatile("s_waitcnt vmcnt(" #n ")" ::: "memory")
; #define PG8_WAIT_L(n) asm volatile("s_waitcnt lgkmcnt(" #n ")" ::: "memory")
; #define PG8_BAR __builtin_amdgcn_s_barrier()
; #define PG8_SCHED __builtin_amdgcn_sched_barrier(0)
;     ...
;             PG8_LDB(B0, 0, 0); PG8_LDB(B1, 0, 1); PG8_SCHED; PG8_LDA(At, 0, 0); PG8_STAGE(PG8_SA(1, 1), a1 + hstepA, voffA);
;             PG8_WAIT_V(8); PG8_WAIT_L(0); PG8_BAR; PG8_MMA(0, 0, At, B0); PG8_MMA(0, 1, At, B1); PG8_BAR; PG8_SCHED;
;             PG8_LDA(At, 0, 1); PG8_STAGE(PG8_SB(0, 0), b2, voffB); PG8_STAGE(PG8_SB(0, 1), b2 + hstepB, voffB); PG8_STAGE(PG8_SA(0, 0), a2, voffA);
;             PG8_WAIT_V(8); PG8_WAIT_L(0); PG8_BAR; PG8_MMA(1, 0, At, B0); PG8_MMA(1, 1, At, B1); PG8_BAR; PG8_SCHED;
.LBB0_922:
	ds_read_b128 v[146:149], v173
	ds_read_b128 v[150:153], v173 offset:1024
	ds_read_b128 v[154:157], v173 offset:2048
	ds_read_b128 v[158:161], v173 offset:3072
	ds_read_b128 v[162:165], v174
	ds_read_b128 v[166:169], v174 offset:1024
	ds_read_b128 v[178:181], v174 offset:2048
	ds_read_b128 v[182:185], v174 offset:3072
	s_add_i32 s67, s30, 2
	s_add_u32 s28, s26, 0x100
	s_addc_u32 s29, s27, 0
	s_cmp_eq_u32 s58, s30
	s_cselect_b32 s30, s24, s65
	s_cselect_b32 s35, s3, s29
	s_cselect_b32 s34, s2, s28
	s_cselect_b32 s31, s25, s66
	v_lshl_add_u64 v[170:171], s[26:27], 0, v[140:141]
	s_add_i32 m0, s46, 0xc000
	ds_read_b128 v[186:189], v175
	ds_read_b128 v[190:193], v175 offset:1024
	ds_read_b128 v[194:197], v175 offset:2048
	ds_read_b128 v[198:201], v175 offset:3072
	ds_read_b128 v[202:205], v175 offset:4096
	ds_read_b128 v[206:209], v175 offset:5120
	ds_read_b128 v[210:213], v175 offset:6144
	ds_read_b128 v[214:217], v175 offset:7168
	global_load_lds_dwordx4 v[170:171], off
	v_lshl_add_u64 v[170:171], s[26:27], 0, v[138:139]
	s_add_i32 m0, s46, 0xe000
	s_nop 0
	global_load_lds_dwordx4 v[170:171], off
	s_waitcnt vmcnt(8)
	s_waitcnt lgkmcnt(0)
	s_barrier
	s_setprio 1
	s_waitcnt lgkmcnt(0)
	v_mfma_f32_16x16x32_bf16 v[126:129], v[146:149], v[186:189], v[126:129]
	v_mfma_f32_16x16x32_bf16 v[122:125], v[154:157], v[186:189], v[122:125]
	v_mfma_f32_16x16x32_bf16 v[118:121], v[146:149], v[194:197], v[118:121]
	v_mfma_f32_16x16x32_bf16 v[114:117], v[154:157], v[194:197], v[114:117]
	v_mfma_f32_16x16x32_bf16 v[106:109], v[146:149], v[202:205], v[106:109]
	v_mfma_f32_16x16x32_bf16 v[98:101], v[154:157], v[202:205], v[98:101]
	v_mfma_f32_16x16x32_bf16 v[90:93], v[146:149], v[210:213], v[90:93]
	v_mfma_f32_16x16x32_bf16 v[82:85], v[154:157], v[210:213], v[82:85]
	v_mfma_f32_16x16x32_bf16 v[126:129], v[150:153], v[190:193], v[126:129]
	v_mfma_f32_16x16x32_bf16 v[122:125], v[158:161], v[190:193], v[122:125]
	v_mfma_f32_16x16x32_bf16 v[118:121], v[150:153], v[198:201], v[118:121]
	v_mfma_f32_16x16x32_bf16 v[114:117], v[158:161], v[198:201], v[114:117]
	v_mfma_f32_16x16x32_bf16 v[106:109], v[150:153], v[206:209], v[106:109]
	v_mfma_f32_16x16x32_bf16 v[98:101], v[158:161], v[206:209], v[98:101]
	v_mfma_f32_16x16x32_bf16 v[90:93], v[150:153], v[214:217], v[90:93]
	v_mfma_f32_16x16x32_bf16 v[82:85], v[158:161], v[214:217], v[82:85]
	s_setprio 0
	s_setprio 1
	v_mfma_f32_16x16x32_bf16 v[110:113], v[162:165], v[186:189], v[110:113]
	v_mfma_f32_16x16x32_bf16 v[102:105], v[178:181], v[186:189], v[102:105]
	v_mfma_f32_16x16x32_bf16 v[94:97], v[162:165], v[194:197], v[94:97]
	v_mfma_f32_16x16x32_bf16 v[86:89], v[178:181], v[194:197], v[86:89]
	v_mfma_f32_16x16x32_bf16 v[78:81], v[162:165], v[202:205], v[78:81]
	v_mfma_f32_16x16x32_bf16 v[74:77], v[178:181], v[202:205], v[74:77]
	v_mfma_f32_16x16x32_bf16 v[70:73], v[162:165], v[210:213], v[70:73]
	v_mfma_f32_16x16x32_bf16 v[66:69], v[178:181], v[210:213], v[66:69]
	v_mfma_f32_16x16x32_bf16 v[110:113], v[166:169], v[190:193], v[110:113]
	v_mfma_f32_16x16x32_bf16 v[102:105], v[182:185], v[190:193], v[102:105]
	v_mfma_f32_16x16x32_bf16 v[94:97], v[166:169], v[198:201], v[94:97]
	v_mfma_f32_16x16x32_bf16 v[86:89], v[182:185], v[198:201], v[86:89]
	v_mfma_f32_16x16x32_bf16 v[78:81], v[166:169], v[206:209], v[78:81]
	v_mfma_f32_16x16x32_bf16 v[74:77], v[182:185], v[206:209], v[74:77]
	v_mfma_f32_16x16x32_bf16 v[70:73], v[166:169], v[214:217], v[70:73]
	v_mfma_f32_16x16x32_bf16 v[66:69], v[182:185], v[214:217], v[66:69]
	s_setprio 0
	s_barrier
	s_mov_b32 m0, s42
	s_add_u32 s98, s30, 0x80
	s_addc_u32 s99, s31, 0
	s_add_u32 s26, s30, 0x160000
	ds_read_b128 v[186:189], v175 offset:16384
	ds_read_b128 v[190:193], v175 offset:17408
	ds_read_b128 v[194:197], v175 offset:18432
	ds_read_b128 v[198:201], v175 offset:19456
	ds_read_b128 v[202:205], v175 offset:20480
	ds_read_b128 v[206:209], v175 offset:21504
	ds_read_b128 v[210:213], v175 offset:22528
	ds_read_b128 v[214:217], v175 offset:23552
	global_load_lds_dwordx4 v132, s[30:31]
	s_mov_b32 m0, s43
	s_addc_u32 s27, s31, 0
	global_load_lds_dwordx4 v136, s[30:31]
	s_mov_b32 m0, s44
	s_nop 0
	global_load_lds_dwordx4 v132, s[26:27]
	s_mov_b32 m0, s45
	s_nop 0
	global_load_lds_dwordx4 v136, s[26:27]
	s_add_u32 s100, s34, 0x80
	s_addc_u32 s101, s35, 0
	s_mov_b32 m0, s46
	s_nop 0
	global_load_lds_dwordx4 v130, s[34:35]
	s_mov_b32 m0, s47
	s_nop 0
	global_load_lds_dwordx4 v134, s[34:35]
	s_waitcnt vmcnt(8)
	s_waitcnt lgkmcnt(0)
	s_barrier
	s_setprio 1
	s_waitcnt lgkmcnt(0)
	v_mfma_f32_16x16x32_bf16 v[62:65], v[146:149], v[186:189], v[62:65]
	v_mfma_f32_16x16x32_bf16 v[58:61], v[154:157], v[186:189], v[58:61]
	v_mfma_f32_16x16x32_bf16 v[54:57], v[146:149], v[194:197], v[54:57]
	v_mfma_f32_16x16x32_bf16 v[50:53], v[154:157], v[194:197], v[50:53]
	v_mfma_f32_16x16x32_bf16 v[42:45], v[146:149], v[202:205], v[42:45]
	v_mfma_f32_16x16x32_bf16 v[34:37], v[154:157], v[202:205], v[34:37]
	v_mfma_f32_16x16x32_bf16 v[26:29], v[146:149], v[210:213], v[26:29]
	v_mfma_f32_16x16x32_bf16 v[18:21], v[154:157], v[210:213], v[18:21]
	v_mfma_f32_16x16x32_bf16 v[62:65], v[150:153], v[190:193], v[62:65]
	v_mfma_f32_16x16x32_bf16 v[58:61], v[158:161], v[190:193], v[58:61]
	v_mfma_f32_16x16x32_bf16 v[54:57], v[150:153], v[198:201], v[54:57]
	v_mfma_f32_16x16x32_bf16 v[50:53], v[158:161], v[198:201], v[50:53]
	v_mfma_f32_16x16x32_bf16 v[42:45], v[150:153], v[206:209], v[42:45]
	v_mfma_f32_16x16x32_bf16 v[34:37], v[158:161], v[206:209], v[34:37]
	v_mfma_f32_16x16x32_bf16 v[26:29], v[150:153], v[214:217], v[26:29]
	v_mfma_f32_16x16x32_bf16 v[18:21], v[158:161], v[214:217], v[18:21]
	s_setprio 0
	s_setprio 1
	v_mfma_f32_16x16x32_bf16 v[46:49], v[162:165], v[186:189], v[46:49]
	v_mfma_f32_16x16x32_bf16 v[38:41], v[178:181], v[186:189], v[38:41]
	v_mfma_f32_16x16x32_bf16 v[30:33], v[162:165], v[194:197], v[30:33]
	v_mfma_f32_16x16x32_bf16 v[22:25], v[178:181], v[194:197], v[22:25]
	v_mfma_f32_16x16x32_bf16 v[14:17], v[162:165], v[202:205], v[14:17]
	v_mfma_f32_16x16x32_bf16 v[10:13], v[178:181], v[202:205], v[10:13]
	v_mfma_f32_16x16x32_bf16 v[6:9], v[162:165], v[210:213], v[6:9]
	v_mfma_f32_16x16x32_bf16 v[2:5], v[178:181], v[210:213], v[2:5]
	v_mfma_f32_16x16x32_bf16 v[46:49], v[166:169], v[190:193], v[46:49]
	v_mfma_f32_16x16x32_bf16 v[38:41], v[182:185], v[190:193], v[38:41]
	v_mfma_f32_16x16x32_bf16 v[30:33], v[166:169], v[198:201], v[30:33]
	v_mfma_f32_16x16x32_bf16 v[22:25], v[182:185], v[198:201], v[22:25]
	v_mfma_f32_16x16x32_bf16 v[14:17], v[166:169], v[206:209], v[14:17]
	v_mfma_f32_16x16x32_bf16 v[10:13], v[182:185], v[206:209], v[10:13]
	v_mfma_f32_16x16x32_bf16 v[6:9], v[166:169], v[214:217], v[6:9]
	v_mfma_f32_16x16x32_bf16 v[2:5], v[182:185], v[214:217], v[2:5]
	s_setprio 0
	s_barrier
; #define PG8_STAGE(bufoff, gbase, voff) do { _Pragma("unroll") for (int _i = 0; _i < 2; ++_i) \
;         __builtin_amdgcn_global_load_lds((const unsigned*)((const char*)(gbase) + (voff)[_i]), (PG8_LAS unsigned*)(lds + (bufoff) + ldsw + _i * 8192), 16, 0, 0); } while (0)
; #define PG8_LDA(dst, b, h) do { if constexpr (DT != 1) { _Pragma("unroll") for (int m = 0; m < 4; ++m) _Pragma("unroll") for (int k = 0; k < 2; ++k) dst[m][k] = *(const PG8_LAS bf16x8*)(lds + PG8_SA(b, h) + aoff + m * 2048 + k * 1024); } \
;         else { _Pragma("unroll") for (int m = 0; m < 4; ++m) dst##8[m] = ld32(lds + PG8_SA(b, h) + aoff + m * 2048); } } while (0)
; #define PG8_LDB(dst, b, h) do { if constexpr (DT != 1) { _Pragma("unroll") for (int n = 0; n < 2; ++n) _Pragma("unroll") for (int k = 0; k < 2; ++k) dst[n][k] = *(const PG8_LAS bf16x8*)(lds + PG8_SB(b, h) + boff + n * 2048 + k * 1024); } \
;         else { _Pragma("unroll") for (int n = 0; n < 2; ++n) dst##8[n] = ld32(lds + PG8_SB(b, h) + boff + n * 2048); } } while (0)
; #define PG8_WAIT_V(n) asm volatile("s_waitcnt vmcnt(" #n ")" ::: "memory")
; #define PG8_WAIT_L(n) asm volatile("s_waitcnt lgkmcnt(" #n ")" ::: "memory")
; #define PG8_BAR __builtin_amdgcn_s_barrier()
; #define PG8_SCHED __builtin_amdgcn_sched_barrier(0)
;     ...
;             PG8_LDB(B0, 1, 0); PG8_LDB(B1, 1, 1); PG8_SCHED; PG8_LDA(At, 1, 0); PG8_STAGE(PG8_SA(0, 1), a2 + hstepA, voffA);
;             PG8_WAIT_V(8); PG8_WAIT_L(0); PG8_BAR; PG8_MMA(0, 0, At, B0); PG8_MMA(0, 1, At, B1); PG8_BAR; PG8_SCHED;
;             PG8_LDA(At, 1, 1); PG8_STAGE(PG8_SB(1, 0), b3, voffB); PG8_STAGE(PG8_SB(1, 1), b3 + hstepB, voffB); PG8_STAGE(PG8_SA(1, 0), a3, voffA);
;             PG8_WAIT_V(8); PG8_WAIT_L(0); PG8_BAR; PG8_MMA(1, 0, At, B0); PG8_MMA(1, 1, At, B1); PG8_BAR; PG8_SCHED;
	ds_read_b128 v[146:149], v176
	ds_read_b128 v[150:153], v176 offset:1024
	ds_read_b128 v[154:157], v176 offset:2048
	ds_read_b128 v[158:161], v176 offset:3072
	ds_read_b128 v[162:165], v177
	ds_read_b128 v[166:169], v177 offset:1024
	ds_read_b128 v[178:181], v177 offset:2048
	ds_read_b128 v[182:185], v177 offset:3072
	s_add_u32 s26, s34, 0x160000
	s_addc_u32 s27, s35, 0
	s_mov_b32 m0, s48
	ds_read_b128 v[186:189], v175 offset:32768
	ds_read_b128 v[190:193], v175 offset:33792
	ds_read_b128 v[194:197], v175 offset:34816
	ds_read_b128 v[198:201], v175 offset:35840
	ds_read_b128 v[202:205], v175 offset:36864
	ds_read_b128 v[206:209], v175 offset:37888
	ds_read_b128 v[210:213], v175 offset:38912
	ds_read_b128 v[214:217], v175 offset:39936
	global_load_lds_dwordx4 v130, s[26:27]
	s_mov_b32 m0, s49
	s_nop 0
	global_load_lds_dwordx4 v134, s[26:27]
	s_waitcnt vmcnt(8)
	s_waitcnt lgkmcnt(0)
	s_barrier
	s_setprio 1
	s_waitcnt lgkmcnt(0)
	v_mfma_f32_16x16x32_bf16 v[126:129], v[146:149], v[186:189], v[126:129]
	v_mfma_f32_16x16x32_bf16 v[122:125], v[154:157], v[186:189], v[122:125]
	v_mfma_f32_16x16x32_bf16 v[118:121], v[146:149], v[194:197], v[118:121]
	v_mfma_f32_16x16x32_bf16 v[114:117], v[154:157], v[194:197], v[114:117]
	v_mfma_f32_16x16x32_bf16 v[106:109], v[146:149], v[202:205], v[106:109]
	v_mfma_f32_16x16x32_bf16 v[98:101], v[154:157], v[202:205], v[98:101]
	v_mfma_f32_16x16x32_bf16 v[90:93], v[146:149], v[210:213], v[90:93]
	v_mfma_f32_16x16x32_bf16 v[82:85], v[154:157], v[210:213], v[82:85]
	v_mfma_f32_16x16x32_bf16 v[126:129], v[150:153], v[190:193], v[126:129]
	v_mfma_f32_16x16x32_bf16 v[122:125], v[158:161], v[190:193], v[122:125]
	v_mfma_f32_16x16x32_bf16 v[118:121], v[150:153], v[198:201], v[118:121]
	v_mfma_f32_16x16x32_bf16 v[114:117], v[158:161], v[198:201], v[114:117]
	v_mfma_f32_16x16x32_bf16 v[106:109], v[150:153], v[206:209], v[106:109]
	v_mfma_f32_16x16x32_bf16 v[98:101], v[158:161], v[206:209], v[98:101]
	v_mfma_f32_16x16x32_bf16 v[90:93], v[150:153], v[214:217], v[90:93]
	v_mfma_f32_16x16x32_bf16 v[82:85], v[158:161], v[214:217], v[82:85]
	s_setprio 0
	s_setprio 1
	v_mfma_f32_16x16x32_bf16 v[110:113], v[162:165], v[186:189], v[110:113]
	v_mfma_f32_16x16x32_bf16 v[102:105], v[178:181], v[186:189], v[102:105]
	v_mfma_f32_16x16x32_bf16 v[94:97], v[162:165], v[194:197], v[94:97]
	v_mfma_f32_16x16x32_bf16 v[86:89], v[178:181], v[194:197], v[86:89]
	v_mfma_f32_16x16x32_bf16 v[78:81], v[162:165], v[202:205], v[78:81]
	v_mfma_f32_16x16x32_bf16 v[74:77], v[178:181], v[202:205], v[74:77]
	v_mfma_f32_16x16x32_bf16 v[70:73], v[162:165], v[210:213], v[70:73]
	v_mfma_f32_16x16x32_bf16 v[66:69], v[178:181], v[210:213], v[66:69]
	v_mfma_f32_16x16x32_bf16 v[110:113], v[166:169], v[190:193], v[110:113]
	v_mfma_f32_16x16x32_bf16 v[102:105], v[182:185], v[190:193], v[102:105]
	v_mfma_f32_16x16x32_bf16 v[94:97], v[166:169], v[198:201], v[94:97]
	v_mfma_f32_16x16x32_bf16 v[86:89], v[182:185], v[198:201], v[86:89]
	v_mfma_f32_16x16x32_bf16 v[78:81], v[166:169], v[206:209], v[78:81]
	v_mfma_f32_16x16x32_bf16 v[74:77], v[182:185], v[206:209], v[74:77]
	v_mfma_f32_16x16x32_bf16 v[70:73], v[166:169], v[214:217], v[70:73]
	v_mfma_f32_16x16x32_bf16 v[66:69], v[182:185], v[214:217], v[66:69]
	s_setprio 0
	s_barrier
	s_mov_b32 m0, s52
	s_add_u32 s26, s30, 0x160080
	ds_read_b128 v[186:189], v175 offset:49152
	ds_read_b128 v[190:193], v175 offset:50176
	ds_read_b128 v[194:197], v175 offset:51200
	ds_read_b128 v[198:201], v175 offset:52224
	ds_read_b128 v[202:205], v175 offset:53248
	ds_read_b128 v[206:209], v175 offset:54272
	ds_read_b128 v[210:213], v175 offset:55296
	ds_read_b128 v[214:217], v175 offset:56320
	global_load_lds_dwordx4 v132, s[98:99]
	s_mov_b32 m0, s53
	s_addc_u32 s27, s31, 0
	global_load_lds_dwordx4 v136, s[98:99]
	s_mov_b32 m0, s56
	s_nop 0
	global_load_lds_dwordx4 v132, s[26:27]
	s_mov_b32 m0, s57
	s_nop 0
	global_load_lds_dwordx4 v136, s[26:27]
	s_mov_b32 m0, s54
	s_nop 0
	global_load_lds_dwordx4 v130, s[100:101]
	s_mov_b32 m0, s55
	s_nop 0
	global_load_lds_dwordx4 v134, s[100:101]
	s_waitcnt vmcnt(8)
	s_waitcnt lgkmcnt(0)
	s_barrier
; #define PG8_WAIT_V(n) asm volatile("s_waitcnt vmcnt(" #n ")" ::: "memory")
; #define PG8_WAIT_L(n) asm volatile("s_waitcnt lgkmcnt(" #n ")" ::: "memory")
; #define PG8_BAR __builtin_amdgcn_s_barrier()
; #define PG8_SCHED __builtin_amdgcn_sched_barrier(0)
;     __device__ __forceinline__ void operator()(const f32x4 (&acc)[2][2][4][2], const Unit& u, int wr, int wc, int fr, int fq) const {
;     ...
;                 for (int m = 0; m < 4; ++m) { const size_t off = (size_t)(row0 + ai * HALF + m * 16) * ldc + col0;
; #pragma unroll
;                     for (int bj = 0; bj < 2; ++bj) { const h16x8_t w = wv[m][bj];
;                         const f32x4 b0 = (f32x4){(float)w[0], (float)w[1], (float)w[2], (float)w[3]}, b1 = (f32x4){(float)w[4], (float)w[5], (float)w[6], (float)w[7]};
;                         const f32x4 o0 = b0 + acc[ai][bj][m][0] * s, o1 = b1 + acc[ai][bj][m][1] * s;
;     ...
;             PG8_WAIT_V(8); PG8_WAIT_L(0); PG8_BAR; PG8_MMA(1, 0, At, B0); PG8_MMA(1, 1, At, B1); PG8_BAR; PG8_SCHED;
	s_setprio 1
	s_waitcnt lgkmcnt(0)
	v_mfma_f32_16x16x32_bf16 v[62:65], v[146:149], v[186:189], v[62:65]
	v_mfma_f32_16x16x32_bf16 v[58:61], v[154:157], v[186:189], v[58:61]
	v_mfma_f32_16x16x32_bf16 v[54:57], v[146:149], v[194:197], v[54:57]
	v_mfma_f32_16x16x32_bf16 v[50:53], v[154:157], v[194:197], v[50:53]
	v_mfma_f32_16x16x32_bf16 v[42:45], v[146:149], v[202:205], v[42:45]
	v_mfma_f32_16x16x32_bf16 v[34:37], v[154:157], v[202:205], v[34:37]
	v_mfma_f32_16x16x32_bf16 v[26:29], v[146:149], v[210:213], v[26:29]
	v_mfma_f32_16x16x32_bf16 v[18:21], v[154:157], v[210:213], v[18:21]
	v_mfma_f32_16x16x32_bf16 v[62:65], v[150:153], v[190:193], v[62:65]
	v_mfma_f32_16x16x32_bf16 v[58:61], v[158:161], v[190:193], v[58:61]
	v_mfma_f32_16x16x32_bf16 v[54:57], v[150:153], v[198:201], v[54:57]
	v_mfma_f32_16x16x32_bf16 v[50:53], v[158:161], v[198:201], v[50:53]
	v_mfma_f32_16x16x32_bf16 v[42:45], v[150:153], v[206:209], v[42:45]
	v_mfma_f32_16x16x32_bf16 v[34:37], v[158:161], v[206:209], v[34:37]
	v_mfma_f32_16x16x32_bf16 v[26:29], v[150:153], v[214:217], v[26:29]
	v_mfma_f32_16x16x32_bf16 v[18:21], v[158:161], v[214:217], v[18:21]
	s_setprio 0
	s_setprio 1
	v_mfma_f32_16x16x32_bf16 v[46:49], v[162:165], v[186:189], v[46:49]
	v_mfma_f32_16x16x32_bf16 v[38:41], v[178:181], v[186:189], v[38:41]
	v_mfma_f32_16x16x32_bf16 v[30:33], v[162:165], v[194:197], v[30:33]
	v_mfma_f32_16x16x32_bf16 v[22:25], v[178:181], v[194:197], v[22:25]
	v_mfma_f32_16x16x32_bf16 v[14:17], v[162:165], v[202:205], v[14:17]
	v_mfma_f32_16x16x32_bf16 v[10:13], v[178:181], v[202:205], v[10:13]
	v_mfma_f32_16x16x32_bf16 v[6:9], v[162:165], v[210:213], v[6:9]
	v_mfma_f32_16x16x32_bf16 v[2:5], v[178:181], v[210:213], v[2:5]
	v_mfma_f32_16x16x32_bf16 v[46:49], v[166:169], v[190:193], v[46:49]
	v_mfma_f32_16x16x32_bf16 v[38:41], v[182:185], v[190:193], v[38:41]
	v_mfma_f32_16x16x32_bf16 v[30:33], v[166:169], v[198:201], v[30:33]
	v_mfma_f32_16x16x32_bf16 v[22:25], v[182:185], v[198:201], v[22:25]
	v_mfma_f32_16x16x32_bf16 v[14:17], v[166:169], v[206:209], v[14:17]
	v_mfma_f32_16x16x32_bf16 v[10:13], v[182:185], v[206:209], v[10:13]
	v_mfma_f32_16x16x32_bf16 v[6:9], v[166:169], v[214:217], v[6:9]
	v_mfma_f32_16x16x32_bf16 v[2:5], v[182:185], v[214:217], v[2:5]
	s_setprio 0
	s_barrier
	s_add_u32 s65, s65, 0x100
	s_addc_u32 s66, s66, 0
	s_cmp_ge_i32 s67, s51
	s_mov_b64 s[26:27], s[28:29]
	s_mov_b32 s30, s67
	s_cbranch_scc0 .LBB0_922
	v_pk_mul_f32 v[128:129], v[128:129], 0.5 op_sel_hi:[1,0]
	v_pk_mul_f32 v[126:127], v[126:127], 0.5 op_sel_hi:[1,0]
	v_pk_mul_f32 v[124:125], v[124:125], 0.5 op_sel_hi:[1,0]
	v_pk_mul_f32 v[122:123], v[122:123], 0.5 op_sel_hi:[1,0]
	v_pk_mul_f32 v[152:153], v[112:113], 0.5 op_sel_hi:[1,0]
	v_pk_mul_f32 v[154:155], v[110:111], 0.5 op_sel_hi:[1,0]
	v_pk_mul_f32 v[156:157], v[104:105], 0.5 op_sel_hi:[1,0]
	v_pk_mul_f32 v[158:159], v[102:103], 0.5 op_sel_hi:[1,0]
	v_pk_mul_f32 v[120:121], v[120:121], 0.5 op_sel_hi:[1,0]
	v_pk_mul_f32 v[118:119], v[118:119], 0.5 op_sel_hi:[1,0]
	v_pk_mul_f32 v[116:117], v[116:117], 0.5 op_sel_hi:[1,0]
	v_pk_mul_f32 v[114:115], v[114:115], 0.5 op_sel_hi:[1,0]
	v_pk_mul_f32 v[160:161], v[96:97], 0.5 op_sel_hi:[1,0]
	v_pk_mul_f32 v[146:147], v[94:95], 0.5 op_sel_hi:[1,0]
	v_pk_mul_f32 v[150:151], v[88:89], 0.5 op_sel_hi:[1,0]
	v_pk_mul_f32 v[148:149], v[86:87], 0.5 op_sel_hi:[1,0]
	v_pk_mul_f32 v[94:95], v[108:109], 0.5 op_sel_hi:[1,0]
	v_pk_mul_f32 v[96:97], v[106:107], 0.5 op_sel_hi:[1,0]
	v_pk_mul_f32 v[100:101], v[100:101], 0.5 op_sel_hi:[1,0]
	v_pk_mul_f32 v[98:99], v[98:99], 0.5 op_sel_hi:[1,0]
	v_pk_mul_f32 v[106:107], v[80:81], 0.5 op_sel_hi:[1,0]
	v_pk_mul_f32 v[108:109], v[78:79], 0.5 op_sel_hi:[1,0]
	v_pk_mul_f32 v[110:111], v[76:77], 0.5 op_sel_hi:[1,0]
	v_pk_mul_f32 v[112:113], v[74:75], 0.5 op_sel_hi:[1,0]
	v_pk_mul_f32 v[74:75], v[92:93], 0.5 op_sel_hi:[1,0]
	v_pk_mul_f32 v[86:87], v[90:91], 0.5 op_sel_hi:[1,0]
	v_pk_mul_f32 v[84:85], v[84:85], 0.5 op_sel_hi:[1,0]
	v_pk_mul_f32 v[88:89], v[82:83], 0.5 op_sel_hi:[1,0]
	v_pk_mul_f32 v[90:91], v[72:73], 0.5 op_sel_hi:[1,0]
	v_pk_mul_f32 v[92:93], v[70:71], 0.5 op_sel_hi:[1,0]
	v_pk_mul_f32 v[102:103], v[68:69], 0.5 op_sel_hi:[1,0]
	v_pk_mul_f32 v[104:105], v[66:67], 0.5 op_sel_hi:[1,0]
	v_pk_mul_f32 v[72:73], v[64:65], 0.5 op_sel_hi:[1,0]
	v_pk_mul_f32 v[70:71], v[62:63], 0.5 op_sel_hi:[1,0]
	v_pk_mul_f32 v[82:83], v[60:61], 0.5 op_sel_hi:[1,0]
	v_pk_mul_f32 v[80:81], v[58:59], 0.5 op_sel_hi:[1,0]
	v_pk_mul_f32 v[68:69], v[48:49], 0.5 op_sel_hi:[1,0]
	v_pk_mul_f32 v[66:67], v[46:47], 0.5 op_sel_hi:[1,0]
	v_pk_mul_f32 v[78:79], v[40:41], 0.5 op_sel_hi:[1,0]
	v_pk_mul_f32 v[76:77], v[38:39], 0.5 op_sel_hi:[1,0]
	v_pk_mul_f32 v[56:57], v[56:57], 0.5 op_sel_hi:[1,0]
	v_pk_mul_f32 v[54:55], v[54:55], 0.5 op_sel_hi:[1,0]
	v_pk_mul_f32 v[64:65], v[52:53], 0.5 op_sel_hi:[1,0]
	v_pk_mul_f32 v[62:63], v[50:51], 0.5 op_sel_hi:[1,0]
	v_pk_mul_f32 v[52:53], v[32:33], 0.5 op_sel_hi:[1,0]
	v_pk_mul_f32 v[50:51], v[30:31], 0.5 op_sel_hi:[1,0]
	v_pk_mul_f32 v[60:61], v[24:25], 0.5 op_sel_hi:[1,0]
	v_pk_mul_f32 v[58:59], v[22:23], 0.5 op_sel_hi:[1,0]
	v_pk_mul_f32 v[40:41], v[44:45], 0.5 op_sel_hi:[1,0]
	v_pk_mul_f32 v[38:39], v[42:43], 0.5 op_sel_hi:[1,0]
	v_pk_mul_f32 v[48:49], v[36:37], 0.5 op_sel_hi:[1,0]
	v_pk_mul_f32 v[46:47], v[34:35], 0.5 op_sel_hi:[1,0]
	v_pk_mul_f32 v[36:37], v[16:17], 0.5 op_sel_hi:[1,0]
	v_pk_mul_f32 v[34:35], v[14:15], 0.5 op_sel_hi:[1,0]
	v_pk_mul_f32 v[44:45], v[12:13], 0.5 op_sel_hi:[1,0]
	v_pk_mul_f32 v[42:43], v[10:11], 0.5 op_sel_hi:[1,0]
	v_pk_mul_f32 v[24:25], v[28:29], 0.5 op_sel_hi:[1,0]
	v_pk_mul_f32 v[22:23], v[26:27], 0.5 op_sel_hi:[1,0]
	v_pk_mul_f32 v[32:33], v[20:21], 0.5 op_sel_hi:[1,0]
	v_pk_mul_f32 v[30:31], v[18:19], 0.5 op_sel_hi:[1,0]
	v_pk_mul_f32 v[20:21], v[8:9], 0.5 op_sel_hi:[1,0]
	v_pk_mul_f32 v[18:19], v[6:7], 0.5 op_sel_hi:[1,0]
	v_pk_mul_f32 v[28:29], v[4:5], 0.5 op_sel_hi:[1,0]
	v_pk_mul_f32 v[26:27], v[2:3], 0.5 op_sel_hi:[1,0]

; #define PG8_STAGE(bufoff, gbase, voff) do { _Pragma("unroll") for (int _i = 0; _i < 2; ++_i) \
;         __builtin_amdgcn_global_load_lds((const unsigned*)((const char*)(gbase) + (voff)[_i]), (PG8_LAS unsigned*)(lds + (bufoff) + ldsw + _i * 8192), 16, 0, 0); } while (0)
; #define PG8_LDA(dst, b, h) do { if constexpr (DT != 1) { _Pragma("unroll") for (int m = 0; m < 4; ++m) _Pragma("unroll") for (int k = 0; k < 2; ++k) dst[m][k] = *(const PG8_LAS bf16x8*)(lds + PG8_SA(b, h) + aoff + m * 2048 + k * 1024); } \
;         else { _Pragma("unroll") for (int m = 0; m < 4; ++m) dst##8[m] = ld32(lds + PG8_SA(b, h) + aoff + m * 2048); } } while (0)
; #define PG8_LDB(dst, b, h) do { if constexpr (DT != 1) { _Pragma("unroll") for (int n = 0; n < 2; ++n) _Pragma("unroll") for (int k = 0; k < 2; ++k) dst[n][k] = *(const PG8_LAS bf16x8*)(lds + PG8_SB(b, h) + boff + n * 2048 + k * 1024); } \
;         else { _Pragma("unroll") for (int n = 0; n < 2; ++n) dst##8[n] = ld32(lds + PG8_SB(b, h) + boff + n * 2048); } } while (0)
; #define PG8_WAIT_V(n) asm volatile("s_waitcnt vmcnt(" #n ")" ::: "memory")
; #define PG8_WAIT_L(n) asm volatile("s_waitcnt lgkmcnt(" #n ")" ::: "memory")
; #define PG8_BAR __builtin_amdgcn_s_barrier()
; #define PG8_SCHED __builtin_amdgcn_sched_barrier(0)
;     ...
;             PG8_LDB(B0, 0, 0); PG8_LDB(B1, 0, 1); PG8_SCHED; PG8_LDA(At, 0, 0); PG8_STAGE(PG8_SA(1, 1), a1 + hstepA, voffA);
;             PG8_WAIT_V(8); PG8_WAIT_L(0); PG8_BAR; PG8_MMA(0, 0, At, B0); PG8_MMA(0, 1, At, B1); PG8_BAR; PG8_SCHED;
;             PG8_LDA(At, 0, 1); PG8_STAGE(PG8_SB(0, 0), b2, voffB); PG8_STAGE(PG8_SB(0, 1), b2 + hstepB, voffB); PG8_STAGE(PG8_SA(0, 0), a2, voffA);
;             PG8_WAIT_V(8); PG8_WAIT_L(0); PG8_BAR; PG8_MMA(1, 0, At, B0); PG8_MMA(1, 1, At, B1); PG8_BAR; PG8_SCHED;
.LBB0_4217:
	ds_read_b128 v[18:21], v187
	ds_read_b128 v[22:25], v187 offset:16
	ds_read_b128 v[26:29], v187 offset:2048
	ds_read_b128 v[30:33], v187 offset:2064
	ds_read_b128 v[2:5], v188
	ds_read_b128 v[6:9], v188 offset:16
	ds_read_b128 v[10:13], v188 offset:2048
	ds_read_b128 v[14:17], v188 offset:2064
	s_add_i32 s68, s34, 2
	s_add_u32 s30, s28, 0x100
	s_addc_u32 s31, s29, 0
	s_cmp_eq_u32 s59, s34
	s_cselect_b32 s34, s26, s66
	s_cselect_b32 s37, s3, s31
	s_cselect_b32 s36, s2, s30
	s_cselect_b32 s35, s27, s67
	v_lshl_add_u64 v[218:219], s[28:29], 0, v[172:173]
	s_add_i32 m0, s47, 0xc000
	ds_read_b128 v[178:181], v189
	ds_read_b128 v[182:185], v189 offset:16
	ds_read_b128 v[194:197], v189 offset:2048
	ds_read_b128 v[198:201], v189 offset:2064
	ds_read_b128 v[202:205], v189 offset:4096
	ds_read_b128 v[206:209], v189 offset:4112
	ds_read_b128 v[210:213], v189 offset:6144
	ds_read_b128 v[214:217], v189 offset:6160
	global_load_lds_dwordx4 v[218:219], off
	v_lshl_add_u64 v[218:219], s[28:29], 0, v[170:171]
	s_add_i32 m0, s47, 0xe000
	s_nop 0
	global_load_lds_dwordx4 v[218:219], off
	s_waitcnt vmcnt(8)
	s_waitcnt lgkmcnt(0)
	s_barrier
	s_setprio 1
	s_waitcnt lgkmcnt(0)
	v_mfma_scale_f32_16x16x128_f8f6f4 v[158:161], v[18:25], v[178:185], v[158:161], v190, v190 op_sel_hi:[0,0,0]
	v_mfma_scale_f32_16x16x128_f8f6f4 v[154:157], v[26:33], v[178:185], v[154:157], v190, v190 op_sel_hi:[0,0,0]
	v_mfma_scale_f32_16x16x128_f8f6f4 v[150:153], v[18:25], v[194:201], v[150:153], v190, v190 op_sel_hi:[0,0,0]
	v_mfma_scale_f32_16x16x128_f8f6f4 v[146:149], v[26:33], v[194:201], v[146:149], v190, v190 op_sel_hi:[0,0,0]
	v_mfma_scale_f32_16x16x128_f8f6f4 v[126:129], v[18:25], v[202:209], v[126:129], v190, v190 op_sel_hi:[0,0,0]
	v_mfma_scale_f32_16x16x128_f8f6f4 v[122:125], v[26:33], v[202:209], v[122:125], v190, v190 op_sel_hi:[0,0,0]
	v_mfma_scale_f32_16x16x128_f8f6f4 v[118:121], v[18:25], v[210:217], v[118:121], v190, v190 op_sel_hi:[0,0,0]
	v_mfma_scale_f32_16x16x128_f8f6f4 v[110:113], v[26:33], v[210:217], v[110:113], v190, v190 op_sel_hi:[0,0,0]
	s_setprio 0
	s_setprio 1
	v_mfma_scale_f32_16x16x128_f8f6f4 v[142:145], v[2:9], v[178:185], v[142:145], v190, v190 op_sel_hi:[0,0,0]
	v_mfma_scale_f32_16x16x128_f8f6f4 v[138:141], v[10:17], v[178:185], v[138:141], v190, v190 op_sel_hi:[0,0,0]
	v_mfma_scale_f32_16x16x128_f8f6f4 v[134:137], v[2:9], v[194:201], v[134:137], v190, v190 op_sel_hi:[0,0,0]
	v_mfma_scale_f32_16x16x128_f8f6f4 v[130:133], v[10:17], v[194:201], v[130:133], v190, v190 op_sel_hi:[0,0,0]
	v_mfma_scale_f32_16x16x128_f8f6f4 v[114:117], v[2:9], v[202:209], v[114:117], v190, v190 op_sel_hi:[0,0,0]
	v_mfma_scale_f32_16x16x128_f8f6f4 v[106:109], v[10:17], v[202:209], v[106:109], v190, v190 op_sel_hi:[0,0,0]
	v_mfma_scale_f32_16x16x128_f8f6f4 v[102:105], v[2:9], v[210:217], v[102:105], v190, v190 op_sel_hi:[0,0,0]
	v_mfma_scale_f32_16x16x128_f8f6f4 v[98:101], v[10:17], v[210:217], v[98:101], v190, v190 op_sel_hi:[0,0,0]
	s_setprio 0
	s_barrier
	s_mov_b32 m0, s43
	s_add_u32 s98, s34, 0x80
	s_addc_u32 s99, s35, 0
	s_add_u32 s28, s34, 0xb0000
	ds_read_b128 v[194:197], v189 offset:16384
	ds_read_b128 v[198:201], v189 offset:16400
	ds_read_b128 v[202:205], v189 offset:18432
	ds_read_b128 v[206:209], v189 offset:18448
	ds_read_b128 v[210:213], v189 offset:20480
	ds_read_b128 v[214:217], v189 offset:20496
	ds_read_b128 v[218:221], v189 offset:22528
	ds_read_b128 v[222:225], v189 offset:22544
	global_load_lds_dwordx4 v164, s[34:35]
	s_mov_b32 m0, s44
	s_addc_u32 s29, s35, 0
	global_load_lds_dwordx4 v168, s[34:35]
	s_mov_b32 m0, s45
	s_nop 0
	global_load_lds_dwordx4 v164, s[28:29]
	s_mov_b32 m0, s46
	s_nop 0
	global_load_lds_dwordx4 v168, s[28:29]
	s_add_u32 s100, s36, 0x80
	s_addc_u32 s101, s37, 0
	s_mov_b32 m0, s47
	s_nop 0
	global_load_lds_dwordx4 v162, s[36:37]
	s_mov_b32 m0, s48
	s_nop 0
	global_load_lds_dwordx4 v166, s[36:37]
	s_waitcnt vmcnt(8)
	s_waitcnt lgkmcnt(0)
	s_barrier
	s_setprio 1
	s_waitcnt lgkmcnt(0)
	v_mfma_scale_f32_16x16x128_f8f6f4 v[94:97], v[18:25], v[194:201], v[94:97], v190, v190 op_sel_hi:[0,0,0]
	v_mfma_scale_f32_16x16x128_f8f6f4 v[90:93], v[26:33], v[194:201], v[90:93], v190, v190 op_sel_hi:[0,0,0]
	v_mfma_scale_f32_16x16x128_f8f6f4 v[78:81], v[18:25], v[202:209], v[78:81], v190, v190 op_sel_hi:[0,0,0]
	v_mfma_scale_f32_16x16x128_f8f6f4 v[74:77], v[26:33], v[202:209], v[74:77], v190, v190 op_sel_hi:[0,0,0]
	v_mfma_scale_f32_16x16x128_f8f6f4 v[226:229], v[18:25], v[210:217], v[62:65], v190, v190 op_sel_hi:[0,0,0]
	v_mfma_scale_f32_16x16x128_f8f6f4 v[230:233], v[26:33], v[210:217], v[58:61], v190, v190 op_sel_hi:[0,0,0]
	v_mfma_scale_f32_16x16x128_f8f6f4 v[234:237], v[18:25], v[218:225], v[46:49], v190, v190 op_sel_hi:[0,0,0]
	v_mfma_scale_f32_16x16x128_f8f6f4 v[238:241], v[26:33], v[218:225], v[42:45], v190, v190 op_sel_hi:[0,0,0]
	s_setprio 0
	s_setprio 1
	v_mfma_scale_f32_16x16x128_f8f6f4 v[86:89], v[2:9], v[194:201], v[86:89], v190, v190 op_sel_hi:[0,0,0]
	v_mfma_scale_f32_16x16x128_f8f6f4 v[82:85], v[10:17], v[194:201], v[82:85], v190, v190 op_sel_hi:[0,0,0]
	v_mfma_scale_f32_16x16x128_f8f6f4 v[70:73], v[2:9], v[202:209], v[70:73], v190, v190 op_sel_hi:[0,0,0]
	v_mfma_scale_f32_16x16x128_f8f6f4 v[66:69], v[10:17], v[202:209], v[66:69], v190, v190 op_sel_hi:[0,0,0]
	v_mfma_scale_f32_16x16x128_f8f6f4 v[242:245], v[2:9], v[210:217], v[54:57], v190, v190 op_sel_hi:[0,0,0]
	v_mfma_scale_f32_16x16x128_f8f6f4 v[210:213], v[10:17], v[210:217], v[50:53], v190, v190 op_sel_hi:[0,0,0]
	v_mfma_scale_f32_16x16x128_f8f6f4 v[214:217], v[2:9], v[218:225], v[38:41], v190, v190 op_sel_hi:[0,0,0]
	v_mfma_scale_f32_16x16x128_f8f6f4 v[218:221], v[10:17], v[218:225], v[34:37], v190, v190 op_sel_hi:[0,0,0]
	s_setprio 0
	s_barrier
; #define PG8_STAGE(bufoff, gbase, voff) do { _Pragma("unroll") for (int _i = 0; _i < 2; ++_i) \
;         __builtin_amdgcn_global_load_lds((const unsigned*)((const char*)(gbase) + (voff)[_i]), (PG8_LAS unsigned*)(lds + (bufoff) + ldsw + _i * 8192), 16, 0, 0); } while (0)
; #define PG8_LDA(dst, b, h) do { if constexpr (DT != 1) { _Pragma("unroll") for (int m = 0; m < 4; ++m) _Pragma("unroll") for (int k = 0; k < 2; ++k) dst[m][k] = *(const PG8_LAS bf16x8*)(lds + PG8_SA(b, h) + aoff + m * 2048 + k * 1024); } \
;         else { _Pragma("unroll") for (int m = 0; m < 4; ++m) dst##8[m] = ld32(lds + PG8_SA(b, h) + aoff + m * 2048); } } while (0)
; #define PG8_LDB(dst, b, h) do { if constexpr (DT != 1) { _Pragma("unroll") for (int n = 0; n < 2; ++n) _Pragma("unroll") for (int k = 0; k < 2; ++k) dst[n][k] = *(const PG8_LAS bf16x8*)(lds + PG8_SB(b, h) + boff + n * 2048 + k * 1024); } \
;         else { _Pragma("unroll") for (int n = 0; n < 2; ++n) dst##8[n] = ld32(lds + PG8_SB(b, h) + boff + n * 2048); } } while (0)
; #define PG8_WAIT_V(n) asm volatile("s_waitcnt vmcnt(" #n ")" ::: "memory")
; #define PG8_WAIT_L(n) asm volatile("s_waitcnt lgkmcnt(" #n ")" ::: "memory")
; #define PG8_BAR __builtin_amdgcn_s_barrier()
; #define PG8_SCHED __builtin_amdgcn_sched_barrier(0)
;     ...
;             PG8_LDB(B0, 1, 0); PG8_LDB(B1, 1, 1); PG8_SCHED; PG8_LDA(At, 1, 0); PG8_STAGE(PG8_SA(0, 1), a2 + hstepA, voffA);
;             PG8_WAIT_V(8); PG8_WAIT_L(0); PG8_BAR; PG8_MMA(0, 0, At, B0); PG8_MMA(0, 1, At, B1); PG8_BAR; PG8_SCHED;
;             PG8_LDA(At, 1, 1); PG8_STAGE(PG8_SB(1, 0), b3, voffB); PG8_STAGE(PG8_SB(1, 1), b3 + hstepB, voffB); PG8_STAGE(PG8_SA(1, 0), a3, voffA);
;             PG8_WAIT_V(8); PG8_WAIT_L(0); PG8_BAR; PG8_MMA(1, 0, At, B0); PG8_MMA(1, 1, At, B1); PG8_BAR; PG8_SCHED;
	ds_read_b128 v[2:5], v191
	ds_read_b128 v[6:9], v191 offset:16
	ds_read_b128 v[10:13], v191 offset:2048
	ds_read_b128 v[14:17], v191 offset:2064
	ds_read_b128 v[18:21], v192
	ds_read_b128 v[22:25], v192 offset:16
	ds_read_b128 v[26:29], v192 offset:2048
	ds_read_b128 v[30:33], v192 offset:2064
	s_add_u32 s28, s36, 0xb0000
	s_addc_u32 s29, s37, 0
	s_mov_b32 m0, s49
	ds_read_b128 v[34:37], v189 offset:32768
	ds_read_b128 v[38:41], v189 offset:32784
	ds_read_b128 v[42:45], v189 offset:34816
	ds_read_b128 v[46:49], v189 offset:34832
	ds_read_b128 v[50:53], v189 offset:36864
	ds_read_b128 v[54:57], v189 offset:36880
	ds_read_b128 v[58:61], v189 offset:38912
	ds_read_b128 v[62:65], v189 offset:38928
	global_load_lds_dwordx4 v162, s[28:29]
	s_mov_b32 m0, s50
	s_nop 0
	global_load_lds_dwordx4 v166, s[28:29]
	s_waitcnt vmcnt(8)
	s_waitcnt lgkmcnt(0)
	s_barrier
	s_setprio 1
	s_waitcnt lgkmcnt(0)
	v_mfma_scale_f32_16x16x128_f8f6f4 v[158:161], v[2:9], v[34:41], v[158:161], v190, v190 op_sel_hi:[0,0,0]
	v_mfma_scale_f32_16x16x128_f8f6f4 v[154:157], v[10:17], v[34:41], v[154:157], v190, v190 op_sel_hi:[0,0,0]
	v_mfma_scale_f32_16x16x128_f8f6f4 v[150:153], v[2:9], v[42:49], v[150:153], v190, v190 op_sel_hi:[0,0,0]
	v_mfma_scale_f32_16x16x128_f8f6f4 v[146:149], v[10:17], v[42:49], v[146:149], v190, v190 op_sel_hi:[0,0,0]
	v_mfma_scale_f32_16x16x128_f8f6f4 v[126:129], v[2:9], v[50:57], v[126:129], v190, v190 op_sel_hi:[0,0,0]
	v_mfma_scale_f32_16x16x128_f8f6f4 v[122:125], v[10:17], v[50:57], v[122:125], v190, v190 op_sel_hi:[0,0,0]
	v_mfma_scale_f32_16x16x128_f8f6f4 v[118:121], v[2:9], v[58:65], v[118:121], v190, v190 op_sel_hi:[0,0,0]
	v_mfma_scale_f32_16x16x128_f8f6f4 v[110:113], v[10:17], v[58:65], v[110:113], v190, v190 op_sel_hi:[0,0,0]
	s_setprio 0
	s_setprio 1
	v_mfma_scale_f32_16x16x128_f8f6f4 v[142:145], v[18:25], v[34:41], v[142:145], v190, v190 op_sel_hi:[0,0,0]
	v_mfma_scale_f32_16x16x128_f8f6f4 v[138:141], v[26:33], v[34:41], v[138:141], v190, v190 op_sel_hi:[0,0,0]
	v_mfma_scale_f32_16x16x128_f8f6f4 v[134:137], v[18:25], v[42:49], v[134:137], v190, v190 op_sel_hi:[0,0,0]
	v_mfma_scale_f32_16x16x128_f8f6f4 v[130:133], v[26:33], v[42:49], v[130:133], v190, v190 op_sel_hi:[0,0,0]
	v_mfma_scale_f32_16x16x128_f8f6f4 v[114:117], v[18:25], v[50:57], v[114:117], v190, v190 op_sel_hi:[0,0,0]
	v_mfma_scale_f32_16x16x128_f8f6f4 v[106:109], v[26:33], v[50:57], v[106:109], v190, v190 op_sel_hi:[0,0,0]
	v_mfma_scale_f32_16x16x128_f8f6f4 v[102:105], v[18:25], v[58:65], v[102:105], v190, v190 op_sel_hi:[0,0,0]
	v_mfma_scale_f32_16x16x128_f8f6f4 v[98:101], v[26:33], v[58:65], v[98:101], v190, v190 op_sel_hi:[0,0,0]
	s_setprio 0
	s_barrier
	s_mov_b32 m0, s53
	s_add_u32 s28, s34, 0xb0080
	ds_read_b128 v[34:37], v189 offset:49152
	ds_read_b128 v[38:41], v189 offset:49168
	ds_read_b128 v[50:53], v189 offset:51200
	ds_read_b128 v[54:57], v189 offset:51216
	ds_read_b128 v[194:197], v189 offset:53248
	ds_read_b128 v[198:201], v189 offset:53264
	ds_read_b128 v[202:205], v189 offset:55296
	ds_read_b128 v[206:209], v189 offset:55312
	global_load_lds_dwordx4 v164, s[98:99]
	s_mov_b32 m0, s54
	s_addc_u32 s29, s35, 0
	global_load_lds_dwordx4 v168, s[98:99]
	s_mov_b32 m0, s57
	s_nop 0
	global_load_lds_dwordx4 v164, s[28:29]
	s_mov_b32 m0, s58
	s_nop 0
	global_load_lds_dwordx4 v168, s[28:29]
	s_mov_b32 m0, s55
	s_nop 0
	global_load_lds_dwordx4 v162, s[100:101]
	s_mov_b32 m0, s56
	s_nop 0
	global_load_lds_dwordx4 v166, s[100:101]
	s_waitcnt vmcnt(8)
	s_waitcnt lgkmcnt(0)
	s_barrier
	s_setprio 1
	s_waitcnt lgkmcnt(0)
	v_mfma_scale_f32_16x16x128_f8f6f4 v[94:97], v[2:9], v[34:41], v[94:97], v190, v190 op_sel_hi:[0,0,0]
	v_mfma_scale_f32_16x16x128_f8f6f4 v[90:93], v[10:17], v[34:41], v[90:93], v190, v190 op_sel_hi:[0,0,0]
	v_mfma_scale_f32_16x16x128_f8f6f4 v[78:81], v[2:9], v[50:57], v[78:81], v190, v190 op_sel_hi:[0,0,0]
	v_mfma_scale_f32_16x16x128_f8f6f4 v[74:77], v[10:17], v[50:57], v[74:77], v190, v190 op_sel_hi:[0,0,0]
	v_mfma_scale_f32_16x16x128_f8f6f4 v[62:65], v[2:9], v[194:201], v[226:229], v190, v190 op_sel_hi:[0,0,0]
	v_mfma_scale_f32_16x16x128_f8f6f4 v[58:61], v[10:17], v[194:201], v[230:233], v190, v190 op_sel_hi:[0,0,0]
	v_mfma_scale_f32_16x16x128_f8f6f4 v[46:49], v[2:9], v[202:209], v[234:237], v190, v190 op_sel_hi:[0,0,0]
	v_mfma_scale_f32_16x16x128_f8f6f4 v[42:45], v[10:17], v[202:209], v[238:241], v190, v190 op_sel_hi:[0,0,0]
	s_setprio 0
	s_setprio 1
	v_mfma_scale_f32_16x16x128_f8f6f4 v[86:89], v[18:25], v[34:41], v[86:89], v190, v190 op_sel_hi:[0,0,0]
	v_mfma_scale_f32_16x16x128_f8f6f4 v[82:85], v[26:33], v[34:41], v[82:85], v190, v190 op_sel_hi:[0,0,0]
	v_mfma_scale_f32_16x16x128_f8f6f4 v[70:73], v[18:25], v[50:57], v[70:73], v190, v190 op_sel_hi:[0,0,0]
	v_mfma_scale_f32_16x16x128_f8f6f4 v[66:69], v[26:33], v[50:57], v[66:69], v190, v190 op_sel_hi:[0,0,0]
	v_mfma_scale_f32_16x16x128_f8f6f4 v[54:57], v[18:25], v[194:201], v[242:245], v190, v190 op_sel_hi:[0,0,0]
	v_mfma_scale_f32_16x16x128_f8f6f4 v[50:53], v[26:33], v[194:201], v[210:213], v190, v190 op_sel_hi:[0,0,0]
	v_mfma_scale_f32_16x16x128_f8f6f4 v[38:41], v[18:25], v[202:209], v[214:217], v190, v190 op_sel_hi:[0,0,0]
	v_mfma_scale_f32_16x16x128_f8f6f4 v[34:37], v[26:33], v[202:209], v[218:221], v190, v190 op_sel_hi:[0,0,0]
	s_setprio 0
	s_barrier
	s_add_u32 s66, s66, 0x100
	s_addc_u32 s67, s67, 0
	s_cmp_ge_i32 s68, s52
	s_mov_b64 s[28:29], s[30:31]
	s_mov_b32 s34, s68
	s_cbranch_scc0 .LBB0_4217

; #define PG8_STAGE(bufoff, gbase, voff) do { _Pragma("unroll") for (int _i = 0; _i < 2; ++_i) \
;         __builtin_amdgcn_global_load_lds((const unsigned*)((const char*)(gbase) + (voff)[_i]), (PG8_LAS unsigned*)(lds + (bufoff) + ldsw + _i * 8192), 16, 0, 0); } while (0)
; #define PG8_LDA(dst, b, h) do { if constexpr (DT != 1) { _Pragma("unroll") for (int m = 0; m < 4; ++m) _Pragma("unroll") for (int k = 0; k < 2; ++k) dst[m][k] = *(const PG8_LAS bf16x8*)(lds + PG8_SA(b, h) + aoff + m * 2048 + k * 1024); } \
;         else { _Pragma("unroll") for (int m = 0; m < 4; ++m) dst##8[m] = ld32(lds + PG8_SA(b, h) + aoff + m * 2048); } } while (0)
; #define PG8_LDB(dst, b, h) do { if constexpr (DT != 1) { _Pragma("unroll") for (int n = 0; n < 2; ++n) _Pragma("unroll") for (int k = 0; k < 2; ++k) dst[n][k] = *(const PG8_LAS bf16x8*)(lds + PG8_SB(b, h) + boff + n * 2048 + k * 1024); } \
;         else { _Pragma("unroll") for (int n = 0; n < 2; ++n) dst##8[n] = ld32(lds + PG8_SB(b, h) + boff + n * 2048); } } while (0)
; #define PG8_WAIT_V(n) asm volatile("s_waitcnt vmcnt(" #n ")" ::: "memory")
; #define PG8_WAIT_L(n) asm volatile("s_waitcnt lgkmcnt(" #n ")" ::: "memory")
; #define PG8_BAR __builtin_amdgcn_s_barrier()
; #define PG8_SCHED __builtin_amdgcn_sched_barrier(0)
;     ...
;             PG8_LDB(B0, 0, 0); PG8_LDB(B1, 0, 1); PG8_SCHED; PG8_LDA(At, 0, 0); PG8_STAGE(PG8_SA(1, 1), a1 + hstepA, voffA);
;             PG8_WAIT_V(8); PG8_WAIT_L(0); PG8_BAR; PG8_MMA(0, 0, At, B0); PG8_MMA(0, 1, At, B1); PG8_BAR; PG8_SCHED;
;             PG8_LDA(At, 0, 1); PG8_STAGE(PG8_SB(0, 0), b2, voffB); PG8_STAGE(PG8_SB(0, 1), b2 + hstepB, voffB); PG8_STAGE(PG8_SA(0, 0), a2, voffA);
;             PG8_WAIT_V(8); PG8_WAIT_L(0); PG8_BAR; PG8_MMA(1, 0, At, B0); PG8_MMA(1, 1, At, B1); PG8_BAR; PG8_SCHED;
.LBB0_4855:
	ds_read_b128 v[16:19], v186
	ds_read_b128 v[20:23], v186 offset:16
	ds_read_b128 v[24:27], v186 offset:2048
	ds_read_b128 v[28:31], v186 offset:2064
	ds_read_b128 v[0:3], v187
	ds_read_b128 v[4:7], v187 offset:16
	ds_read_b128 v[8:11], v187 offset:2048
	ds_read_b128 v[12:15], v187 offset:2064
	s_add_i32 s61, s26, 2
	s_add_u32 s24, s22, 0x100
	s_addc_u32 s25, s23, 0
	s_cmp_eq_u32 s52, s26
	s_cselect_b32 s26, s20, s59
	s_cselect_b32 s29, s3, s25
	s_cselect_b32 s28, s2, s24
	s_cselect_b32 s27, s21, s60
	v_lshl_add_u64 v[216:217], s[22:23], 0, v[170:171]
	s_add_i32 m0, s40, 0xc000
	ds_read_b128 v[176:179], v188
	ds_read_b128 v[180:183], v188 offset:16
	ds_read_b128 v[192:195], v188 offset:2048
	ds_read_b128 v[196:199], v188 offset:2064
	ds_read_b128 v[200:203], v188 offset:4096
	ds_read_b128 v[204:207], v188 offset:4112
	ds_read_b128 v[208:211], v188 offset:6144
	ds_read_b128 v[212:215], v188 offset:6160
	global_load_lds_dwordx4 v[216:217], off
	v_lshl_add_u64 v[216:217], s[22:23], 0, v[168:169]
	s_add_i32 m0, s40, 0xe000
	s_nop 0
	global_load_lds_dwordx4 v[216:217], off
	s_waitcnt vmcnt(8)
	s_waitcnt lgkmcnt(0)
	s_barrier
	s_setprio 1
	s_waitcnt lgkmcnt(0)
	v_mfma_scale_f32_16x16x128_f8f6f4 v[156:159], v[16:23], v[176:183], v[156:159], v189, v189 op_sel_hi:[0,0,0]
	v_mfma_scale_f32_16x16x128_f8f6f4 v[152:155], v[24:31], v[176:183], v[152:155], v189, v189 op_sel_hi:[0,0,0]
	v_mfma_scale_f32_16x16x128_f8f6f4 v[148:151], v[16:23], v[192:199], v[148:151], v189, v189 op_sel_hi:[0,0,0]
	v_mfma_scale_f32_16x16x128_f8f6f4 v[144:147], v[24:31], v[192:199], v[144:147], v189, v189 op_sel_hi:[0,0,0]
	v_mfma_scale_f32_16x16x128_f8f6f4 v[128:131], v[16:23], v[200:207], v[128:131], v189, v189 op_sel_hi:[0,0,0]
	v_mfma_scale_f32_16x16x128_f8f6f4 v[120:123], v[24:31], v[200:207], v[120:123], v189, v189 op_sel_hi:[0,0,0]
	v_mfma_scale_f32_16x16x128_f8f6f4 v[108:111], v[16:23], v[208:215], v[108:111], v189, v189 op_sel_hi:[0,0,0]
	v_mfma_scale_f32_16x16x128_f8f6f4 v[104:107], v[24:31], v[208:215], v[104:107], v189, v189 op_sel_hi:[0,0,0]
	s_setprio 0
	s_setprio 1
	v_mfma_scale_f32_16x16x128_f8f6f4 v[140:143], v[0:7], v[176:183], v[140:143], v189, v189 op_sel_hi:[0,0,0]
	v_mfma_scale_f32_16x16x128_f8f6f4 v[136:139], v[8:15], v[176:183], v[136:139], v189, v189 op_sel_hi:[0,0,0]
	v_mfma_scale_f32_16x16x128_f8f6f4 v[132:135], v[0:7], v[192:199], v[132:135], v189, v189 op_sel_hi:[0,0,0]
	v_mfma_scale_f32_16x16x128_f8f6f4 v[124:127], v[8:15], v[192:199], v[124:127], v189, v189 op_sel_hi:[0,0,0]
	v_mfma_scale_f32_16x16x128_f8f6f4 v[116:119], v[0:7], v[200:207], v[116:119], v189, v189 op_sel_hi:[0,0,0]
	v_mfma_scale_f32_16x16x128_f8f6f4 v[112:115], v[8:15], v[200:207], v[112:115], v189, v189 op_sel_hi:[0,0,0]
	v_mfma_scale_f32_16x16x128_f8f6f4 v[100:103], v[0:7], v[208:215], v[100:103], v189, v189 op_sel_hi:[0,0,0]
	v_mfma_scale_f32_16x16x128_f8f6f4 v[96:99], v[8:15], v[208:215], v[96:99], v189, v189 op_sel_hi:[0,0,0]
	s_setprio 0
	s_barrier
	s_mov_b32 m0, s36
	s_add_u32 s98, s26, 0x80
	s_addc_u32 s99, s27, 0
	s_add_u32 s22, s26, 0xb0000
	ds_read_b128 v[192:195], v188 offset:16384
	ds_read_b128 v[196:199], v188 offset:16400
	ds_read_b128 v[200:203], v188 offset:18432
	ds_read_b128 v[204:207], v188 offset:18448
	ds_read_b128 v[208:211], v188 offset:20480
	ds_read_b128 v[212:215], v188 offset:20496
	ds_read_b128 v[216:219], v188 offset:22528
	ds_read_b128 v[220:223], v188 offset:22544
	global_load_lds_dwordx4 v162, s[26:27]
	s_mov_b32 m0, s37
	s_addc_u32 s23, s27, 0
	global_load_lds_dwordx4 v166, s[26:27]
	s_mov_b32 m0, s38
	s_nop 0
	global_load_lds_dwordx4 v162, s[22:23]
	s_mov_b32 m0, s39
	s_nop 0
	global_load_lds_dwordx4 v166, s[22:23]
	s_add_u32 s100, s28, 0x80
	s_addc_u32 s101, s29, 0
	s_mov_b32 m0, s40
	s_nop 0
	global_load_lds_dwordx4 v160, s[28:29]
	s_mov_b32 m0, s41
	s_nop 0
	global_load_lds_dwordx4 v164, s[28:29]
	s_waitcnt vmcnt(8)
	s_waitcnt lgkmcnt(0)
	s_barrier
	s_setprio 1
	s_waitcnt lgkmcnt(0)
	v_mfma_scale_f32_16x16x128_f8f6f4 v[92:95], v[16:23], v[192:199], v[92:95], v189, v189 op_sel_hi:[0,0,0]
	v_mfma_scale_f32_16x16x128_f8f6f4 v[88:91], v[24:31], v[192:199], v[88:91], v189, v189 op_sel_hi:[0,0,0]
	v_mfma_scale_f32_16x16x128_f8f6f4 v[76:79], v[16:23], v[200:207], v[76:79], v189, v189 op_sel_hi:[0,0,0]
	v_mfma_scale_f32_16x16x128_f8f6f4 v[72:75], v[24:31], v[200:207], v[72:75], v189, v189 op_sel_hi:[0,0,0]
	v_mfma_scale_f32_16x16x128_f8f6f4 v[224:227], v[16:23], v[208:215], v[60:63], v189, v189 op_sel_hi:[0,0,0]
	v_mfma_scale_f32_16x16x128_f8f6f4 v[228:231], v[24:31], v[208:215], v[56:59], v189, v189 op_sel_hi:[0,0,0]
	v_mfma_scale_f32_16x16x128_f8f6f4 v[232:235], v[16:23], v[216:223], v[44:47], v189, v189 op_sel_hi:[0,0,0]
	v_mfma_scale_f32_16x16x128_f8f6f4 v[236:239], v[24:31], v[216:223], v[40:43], v189, v189 op_sel_hi:[0,0,0]
	s_setprio 0
	s_setprio 1
	v_mfma_scale_f32_16x16x128_f8f6f4 v[84:87], v[0:7], v[192:199], v[84:87], v189, v189 op_sel_hi:[0,0,0]
	v_mfma_scale_f32_16x16x128_f8f6f4 v[80:83], v[8:15], v[192:199], v[80:83], v189, v189 op_sel_hi:[0,0,0]
	v_mfma_scale_f32_16x16x128_f8f6f4 v[68:71], v[0:7], v[200:207], v[68:71], v189, v189 op_sel_hi:[0,0,0]
	v_mfma_scale_f32_16x16x128_f8f6f4 v[64:67], v[8:15], v[200:207], v[64:67], v189, v189 op_sel_hi:[0,0,0]
	v_mfma_scale_f32_16x16x128_f8f6f4 v[240:243], v[0:7], v[208:215], v[52:55], v189, v189 op_sel_hi:[0,0,0]
	v_mfma_scale_f32_16x16x128_f8f6f4 v[208:211], v[8:15], v[208:215], v[48:51], v189, v189 op_sel_hi:[0,0,0]
	v_mfma_scale_f32_16x16x128_f8f6f4 v[212:215], v[0:7], v[216:223], v[36:39], v189, v189 op_sel_hi:[0,0,0]
	v_mfma_scale_f32_16x16x128_f8f6f4 v[216:219], v[8:15], v[216:223], v[32:35], v189, v189 op_sel_hi:[0,0,0]
	s_setprio 0
	s_barrier
; #define PG8_STAGE(bufoff, gbase, voff) do { _Pragma("unroll") for (int _i = 0; _i < 2; ++_i) \
;         __builtin_amdgcn_global_load_lds((const unsigned*)((const char*)(gbase) + (voff)[_i]), (PG8_LAS unsigned*)(lds + (bufoff) + ldsw + _i * 8192), 16, 0, 0); } while (0)
; #define PG8_LDA(dst, b, h) do { if constexpr (DT != 1) { _Pragma("unroll") for (int m = 0; m < 4; ++m) _Pragma("unroll") for (int k = 0; k < 2; ++k) dst[m][k] = *(const PG8_LAS bf16x8*)(lds + PG8_SA(b, h) + aoff + m * 2048 + k * 1024); } \
;         else { _Pragma("unroll") for (int m = 0; m < 4; ++m) dst##8[m] = ld32(lds + PG8_SA(b, h) + aoff + m * 2048); } } while (0)
; #define PG8_LDB(dst, b, h) do { if constexpr (DT != 1) { _Pragma("unroll") for (int n = 0; n < 2; ++n) _Pragma("unroll") for (int k = 0; k < 2; ++k) dst[n][k] = *(const PG8_LAS bf16x8*)(lds + PG8_SB(b, h) + boff + n * 2048 + k * 1024); } \
;         else { _Pragma("unroll") for (int n = 0; n < 2; ++n) dst##8[n] = ld32(lds + PG8_SB(b, h) + boff + n * 2048); } } while (0)
; #define PG8_WAIT_V(n) asm volatile("s_waitcnt vmcnt(" #n ")" ::: "memory")
; #define PG8_WAIT_L(n) asm volatile("s_waitcnt lgkmcnt(" #n ")" ::: "memory")
; #define PG8_BAR __builtin_amdgcn_s_barrier()
; #define PG8_SCHED __builtin_amdgcn_sched_barrier(0)
;     ...
;             PG8_LDB(B0, 1, 0); PG8_LDB(B1, 1, 1); PG8_SCHED; PG8_LDA(At, 1, 0); PG8_STAGE(PG8_SA(0, 1), a2 + hstepA, voffA);
;             PG8_WAIT_V(8); PG8_WAIT_L(0); PG8_BAR; PG8_MMA(0, 0, At, B0); PG8_MMA(0, 1, At, B1); PG8_BAR; PG8_SCHED;
;             PG8_LDA(At, 1, 1); PG8_STAGE(PG8_SB(1, 0), b3, voffB); PG8_STAGE(PG8_SB(1, 1), b3 + hstepB, voffB); PG8_STAGE(PG8_SA(1, 0), a3, voffA);
;             PG8_WAIT_V(8); PG8_WAIT_L(0); PG8_BAR; PG8_MMA(1, 0, At, B0); PG8_MMA(1, 1, At, B1); PG8_BAR; PG8_SCHED;
	ds_read_b128 v[0:3], v190
	ds_read_b128 v[4:7], v190 offset:16
	ds_read_b128 v[8:11], v190 offset:2048
	ds_read_b128 v[12:15], v190 offset:2064
	ds_read_b128 v[16:19], v191
	ds_read_b128 v[20:23], v191 offset:16
	ds_read_b128 v[24:27], v191 offset:2048
	ds_read_b128 v[28:31], v191 offset:2064
	s_add_u32 s22, s28, 0xb0000
	s_addc_u32 s23, s29, 0
	s_mov_b32 m0, s42
	ds_read_b128 v[32:35], v188 offset:32768
	ds_read_b128 v[36:39], v188 offset:32784
	ds_read_b128 v[40:43], v188 offset:34816
	ds_read_b128 v[44:47], v188 offset:34832
	ds_read_b128 v[48:51], v188 offset:36864
	ds_read_b128 v[52:55], v188 offset:36880
	ds_read_b128 v[56:59], v188 offset:38912
	ds_read_b128 v[60:63], v188 offset:38928
	global_load_lds_dwordx4 v160, s[22:23]
	s_mov_b32 m0, s43
	s_nop 0
	global_load_lds_dwordx4 v164, s[22:23]
	s_waitcnt vmcnt(8)
	s_waitcnt lgkmcnt(0)
	s_barrier
	s_setprio 1
	s_waitcnt lgkmcnt(0)
	v_mfma_scale_f32_16x16x128_f8f6f4 v[156:159], v[0:7], v[32:39], v[156:159], v189, v189 op_sel_hi:[0,0,0]
	v_mfma_scale_f32_16x16x128_f8f6f4 v[152:155], v[8:15], v[32:39], v[152:155], v189, v189 op_sel_hi:[0,0,0]
	v_mfma_scale_f32_16x16x128_f8f6f4 v[148:151], v[0:7], v[40:47], v[148:151], v189, v189 op_sel_hi:[0,0,0]
	v_mfma_scale_f32_16x16x128_f8f6f4 v[144:147], v[8:15], v[40:47], v[144:147], v189, v189 op_sel_hi:[0,0,0]
	v_mfma_scale_f32_16x16x128_f8f6f4 v[128:131], v[0:7], v[48:55], v[128:131], v189, v189 op_sel_hi:[0,0,0]
	v_mfma_scale_f32_16x16x128_f8f6f4 v[120:123], v[8:15], v[48:55], v[120:123], v189, v189 op_sel_hi:[0,0,0]
	v_mfma_scale_f32_16x16x128_f8f6f4 v[108:111], v[0:7], v[56:63], v[108:111], v189, v189 op_sel_hi:[0,0,0]
	v_mfma_scale_f32_16x16x128_f8f6f4 v[104:107], v[8:15], v[56:63], v[104:107], v189, v189 op_sel_hi:[0,0,0]
	s_setprio 0
	s_setprio 1
	v_mfma_scale_f32_16x16x128_f8f6f4 v[140:143], v[16:23], v[32:39], v[140:143], v189, v189 op_sel_hi:[0,0,0]
	v_mfma_scale_f32_16x16x128_f8f6f4 v[136:139], v[24:31], v[32:39], v[136:139], v189, v189 op_sel_hi:[0,0,0]
	v_mfma_scale_f32_16x16x128_f8f6f4 v[132:135], v[16:23], v[40:47], v[132:135], v189, v189 op_sel_hi:[0,0,0]
	v_mfma_scale_f32_16x16x128_f8f6f4 v[124:127], v[24:31], v[40:47], v[124:127], v189, v189 op_sel_hi:[0,0,0]
	v_mfma_scale_f32_16x16x128_f8f6f4 v[116:119], v[16:23], v[48:55], v[116:119], v189, v189 op_sel_hi:[0,0,0]
	v_mfma_scale_f32_16x16x128_f8f6f4 v[112:115], v[24:31], v[48:55], v[112:115], v189, v189 op_sel_hi:[0,0,0]
	v_mfma_scale_f32_16x16x128_f8f6f4 v[100:103], v[16:23], v[56:63], v[100:103], v189, v189 op_sel_hi:[0,0,0]
	v_mfma_scale_f32_16x16x128_f8f6f4 v[96:99], v[24:31], v[56:63], v[96:99], v189, v189 op_sel_hi:[0,0,0]
	s_setprio 0
	s_barrier
	s_mov_b32 m0, s46
	s_add_u32 s22, s26, 0xb0080
	ds_read_b128 v[32:35], v188 offset:49152
	ds_read_b128 v[36:39], v188 offset:49168
	ds_read_b128 v[48:51], v188 offset:51200
	ds_read_b128 v[52:55], v188 offset:51216
	ds_read_b128 v[192:195], v188 offset:53248
	ds_read_b128 v[196:199], v188 offset:53264
	ds_read_b128 v[200:203], v188 offset:55296
	ds_read_b128 v[204:207], v188 offset:55312
	global_load_lds_dwordx4 v162, s[98:99]
	s_mov_b32 m0, s47
	s_addc_u32 s23, s27, 0
	global_load_lds_dwordx4 v166, s[98:99]
	s_mov_b32 m0, s50
	s_nop 0
	global_load_lds_dwordx4 v162, s[22:23]
	s_mov_b32 m0, s51
	s_nop 0
	global_load_lds_dwordx4 v166, s[22:23]
	s_mov_b32 m0, s48
	s_nop 0
	global_load_lds_dwordx4 v160, s[100:101]
	s_mov_b32 m0, s49
	s_nop 0
	global_load_lds_dwordx4 v164, s[100:101]
	s_waitcnt vmcnt(8)
	s_waitcnt lgkmcnt(0)
	s_barrier
	s_setprio 1
	s_waitcnt lgkmcnt(0)
	v_mfma_scale_f32_16x16x128_f8f6f4 v[92:95], v[0:7], v[32:39], v[92:95], v189, v189 op_sel_hi:[0,0,0]
	v_mfma_scale_f32_16x16x128_f8f6f4 v[88:91], v[8:15], v[32:39], v[88:91], v189, v189 op_sel_hi:[0,0,0]
	v_mfma_scale_f32_16x16x128_f8f6f4 v[76:79], v[0:7], v[48:55], v[76:79], v189, v189 op_sel_hi:[0,0,0]
	v_mfma_scale_f32_16x16x128_f8f6f4 v[72:75], v[8:15], v[48:55], v[72:75], v189, v189 op_sel_hi:[0,0,0]
	v_mfma_scale_f32_16x16x128_f8f6f4 v[60:63], v[0:7], v[192:199], v[224:227], v189, v189 op_sel_hi:[0,0,0]
	v_mfma_scale_f32_16x16x128_f8f6f4 v[56:59], v[8:15], v[192:199], v[228:231], v189, v189 op_sel_hi:[0,0,0]
	v_mfma_scale_f32_16x16x128_f8f6f4 v[44:47], v[0:7], v[200:207], v[232:235], v189, v189 op_sel_hi:[0,0,0]
	v_mfma_scale_f32_16x16x128_f8f6f4 v[40:43], v[8:15], v[200:207], v[236:239], v189, v189 op_sel_hi:[0,0,0]
	s_setprio 0
	s_setprio 1
	v_mfma_scale_f32_16x16x128_f8f6f4 v[84:87], v[16:23], v[32:39], v[84:87], v189, v189 op_sel_hi:[0,0,0]
	v_mfma_scale_f32_16x16x128_f8f6f4 v[80:83], v[24:31], v[32:39], v[80:83], v189, v189 op_sel_hi:[0,0,0]
	v_mfma_scale_f32_16x16x128_f8f6f4 v[68:71], v[16:23], v[48:55], v[68:71], v189, v189 op_sel_hi:[0,0,0]
	v_mfma_scale_f32_16x16x128_f8f6f4 v[64:67], v[24:31], v[48:55], v[64:67], v189, v189 op_sel_hi:[0,0,0]
	v_mfma_scale_f32_16x16x128_f8f6f4 v[52:55], v[16:23], v[192:199], v[240:243], v189, v189 op_sel_hi:[0,0,0]
	v_mfma_scale_f32_16x16x128_f8f6f4 v[48:51], v[24:31], v[192:199], v[208:211], v189, v189 op_sel_hi:[0,0,0]
	v_mfma_scale_f32_16x16x128_f8f6f4 v[36:39], v[16:23], v[200:207], v[212:215], v189, v189 op_sel_hi:[0,0,0]
	v_mfma_scale_f32_16x16x128_f8f6f4 v[32:35], v[24:31], v[200:207], v[216:219], v189, v189 op_sel_hi:[0,0,0]
	s_setprio 0
	s_barrier
	s_add_u32 s59, s59, 0x100
	s_addc_u32 s60, s60, 0
	s_cmp_ge_i32 s61, s45
	s_mov_b64 s[22:23], s[24:25]
	s_mov_b32 s26, s61
	s_cbranch_scc0 .LBB0_4855
